# speedup vs baseline: 1.0177x; 1.0177x over previous
_Z11pwconv_mfmaPKfPK15HIP_vector_typeIjLj4EES0_Pf:
	s_load_dwordx4 s[12:15], s[0:1], 0x0
	s_load_dwordx4 s[16:19], s[0:1], 0x10
	s_and_b32 s20, s2, 7
	s_lshr_b32 s21, s2, 3
	s_lshr_b32 s37, s20, 1
	s_and_b32 s36, s20, 1
	s_mul_i32 s36, s36, 31
	s_add_i32 s36, s36, s21
	s_lshr_b32 s21, s36, 1
	s_and_b32 s36, s36, 1
	s_lshl_b32 s37, s37, 1
	s_add_i32 s20, s37, s36
	v_lshrrev_b32_e32 v1, 6, v0
	v_and_b32_e32 v2, 63, v0
	s_nop 0
	v_readfirstlane_b32 s22, v1
	s_nop 3
	s_lshl_b32 s23, s20, 3
	s_add_i32 s23, s23, s22
	s_mul_i32 s24, s23, 0x439200
	s_mul_i32 s25, s21, 0x1f0
	s_add_u32 s24, s24, s25
	s_lshl_b32 s25, s21, 17
	s_lshl_b32 s26, s22, 13
	s_add_u32 s25, s25, s26
	s_mul_i32 s27, s20, 0x1e080
	s_mul_i32 s36, s21, 0x1f0
	s_add_u32 s27, s27, s36
	v_min_u32_e32 v10, 61, v2
	v_lshlrev_b32_e32 v3, 3, v10
	v_lshlrev_b32_e32 v4, 4, v2
	v_cmp_lt_u32_e32 vcc, 30, v10
	s_nop 1
	v_cndmask_b32_e64 v5, 0, 1, vcc
	v_mul_u32_u24_e32 v6, 31, v5
	v_sub_u32_e32 v6, v10, v6
	v_lshl_add_u32 v7, v1, 1, v5
	v_and_b32_e32 v8, 7, v6
	v_xor_b32_e32 v7, v7, v8
	v_lshlrev_b32_e32 v7, 4, v7
	v_lshl_add_u32 v5, v6, 12, v7
	s_lshl_b32 s36, s22, 2
	s_add_i32 s36, s36, 0
	s_and_b32 s36, s36, 7
	s_lshl_b32 s37, s22, 14
	s_add_i32 s37, s37, 0x0
	v_xor_b32_e32 v6, s36, v2
	v_lshlrev_b32_e32 v6, 4, v6
	v_add_u32_e32 v6, s37, v6
	s_lshl_b32 s36, s22, 2
	s_add_i32 s36, s36, 1
	s_and_b32 s36, s36, 7
	s_lshl_b32 s37, s22, 14
	s_add_i32 s37, s37, 0x1000
	v_xor_b32_e32 v7, s36, v2
	v_lshlrev_b32_e32 v7, 4, v7
	v_add_u32_e32 v7, s37, v7
	s_lshl_b32 s36, s22, 2
	s_add_i32 s36, s36, 2
	s_and_b32 s36, s36, 7
	s_lshl_b32 s37, s22, 14
	s_add_i32 s37, s37, 0x2000
	v_xor_b32_e32 v8, s36, v2
	v_lshlrev_b32_e32 v8, 4, v8
	v_add_u32_e32 v8, s37, v8
	s_lshl_b32 s36, s22, 2
	s_add_i32 s36, s36, 3
	s_and_b32 s36, s36, 7
	s_lshl_b32 s37, s22, 14
	s_add_i32 s37, s37, 0x3000
	v_xor_b32_e32 v9, s36, v2
	v_lshlrev_b32_e32 v9, 4, v9
	v_add_u32_e32 v9, s37, v9
	s_lshl_b32 s36, s22, 11
	s_add_i32 s36, s36, 0x20000
	v_add_u32_e32 v254, s36, v4
	s_add_i32 s37, s22, 1
	s_min_u32 s37, s37, 7
	s_lshl_b32 s37, s37, 11
	s_add_i32 s37, s37, 0x20000
	v_add_u32_e32 v255, s37, v4
	v_lshrrev_b32_e32 v10, 5, v0
	v_lshrrev_b32_e32 v11, 1, v10
	v_mul_u32_u24_e32 v11, 0x3c10, v11
	v_and_b32_e32 v10, 1, v10
	v_mul_u32_u24_e32 v10, 0xf8, v10
	v_add_u32_e32 v11, v11, v10
	v_and_b32_e32 v10, 31, v0
	v_lshl_add_u32 v11, v10, 3, v11
	v_add_u32_e32 v11, s27, v11
	v_cmp_eq_u32_e32 vcc, 31, v10
	v_mov_b32_e32 v10, 0x7f000000
	s_nop 1
	v_cndmask_b32_e32 v11, v11, v10, vcc
	s_waitcnt lgkmcnt(0)
	s_add_u32 s4, s12, s24
	s_addc_u32 s5, s13, 0
	s_and_b32 s5, s5, 0xffff
	s_sub_u32 s6, 0x10e48000, s24
	s_mov_b32 s7, 0x20000
	s_add_u32 s8, s14, s25
	s_addc_u32 s9, s15, 0
	s_and_b32 s9, s9, 0xffff
	s_sub_u32 s10, 0x400000, s25
	s_mov_b32 s11, 0x20000
	s_mov_b32 s28, s16
	s_and_b32 s29, s17, 0xffff
	s_mov_b32 s30, 0xf0400
	s_mov_b32 s31, 0x20000
	s_mov_b32 s32, s18
	s_and_b32 s33, s19, 0xffff
	s_mov_b32 s34, 0xf04000
	s_mov_b32 s35, 0x20000
	s_mov_b32 s40, 0x0
	s_mov_b32 s41, 0x21c90
	s_mov_b32 s42, 0x43920
	s_mov_b32 s43, 0x655b0
	s_mov_b32 s44, 0x87240
	s_mov_b32 s45, 0xa8ed0
	s_mov_b32 s46, 0xcab60
	s_mov_b32 s47, 0xec7f0
	buffer_load_dwordx2 v[44:45], v3, s[4:7], s40 offen nt
	buffer_load_dwordx2 v[46:47], v3, s[4:7], s41 offen nt
	buffer_load_dwordx2 v[48:49], v3, s[4:7], s42 offen nt
	buffer_load_dwordx2 v[50:51], v3, s[4:7], s43 offen nt
	buffer_load_dwordx2 v[52:53], v3, s[4:7], s44 offen nt
	buffer_load_dwordx2 v[54:55], v3, s[4:7], s45 offen nt
	buffer_load_dwordx2 v[56:57], v3, s[4:7], s46 offen nt
	buffer_load_dwordx2 v[58:59], v3, s[4:7], s47 offen nt
	s_mov_b32 s40, 0x10e480
	s_mov_b32 s41, 0x130110
	s_mov_b32 s42, 0x151da0
	s_mov_b32 s43, 0x173a30
	s_mov_b32 s44, 0x1956c0
	s_mov_b32 s45, 0x1b7350
	s_mov_b32 s46, 0x1d8fe0
	s_mov_b32 s47, 0x1fac70
	buffer_load_dwordx2 v[60:61], v3, s[4:7], s40 offen nt
	buffer_load_dwordx2 v[62:63], v3, s[4:7], s41 offen nt
	buffer_load_dwordx2 v[64:65], v3, s[4:7], s42 offen nt
	buffer_load_dwordx2 v[66:67], v3, s[4:7], s43 offen nt
	buffer_load_dwordx2 v[68:69], v3, s[4:7], s44 offen nt
	buffer_load_dwordx2 v[70:71], v3, s[4:7], s45 offen nt
	buffer_load_dwordx2 v[72:73], v3, s[4:7], s46 offen nt
	buffer_load_dwordx2 v[74:75], v3, s[4:7], s47 offen nt
	s_mov_b32 s40, 0x21c900
	s_mov_b32 s41, 0x23e590
	s_mov_b32 s42, 0x260220
	s_mov_b32 s43, 0x281eb0
	s_mov_b32 s44, 0x2a3b40
	s_mov_b32 s45, 0x2c57d0
	s_mov_b32 s46, 0x2e7460
	s_mov_b32 s47, 0x3090f0
	buffer_load_dwordx2 v[76:77], v3, s[4:7], s40 offen nt
	buffer_load_dwordx2 v[78:79], v3, s[4:7], s41 offen nt
	buffer_load_dwordx2 v[80:81], v3, s[4:7], s42 offen nt
	buffer_load_dwordx2 v[82:83], v3, s[4:7], s43 offen nt
	buffer_load_dwordx2 v[84:85], v3, s[4:7], s44 offen nt
	buffer_load_dwordx2 v[86:87], v3, s[4:7], s45 offen nt
	buffer_load_dwordx2 v[88:89], v3, s[4:7], s46 offen nt
	buffer_load_dwordx2 v[90:91], v3, s[4:7], s47 offen nt
	s_mov_b32 s40, 0x32ad80
	s_mov_b32 s41, 0x34ca10
	s_mov_b32 s42, 0x36e6a0
	s_mov_b32 s43, 0x390330
	s_mov_b32 s44, 0x3b1fc0
	s_mov_b32 s45, 0x3d3c50
	s_mov_b32 s46, 0x3f58e0
	s_mov_b32 s47, 0x417570
	buffer_load_dwordx2 v[92:93], v3, s[4:7], s40 offen nt
	buffer_load_dwordx2 v[94:95], v3, s[4:7], s41 offen nt
	buffer_load_dwordx2 v[96:97], v3, s[4:7], s42 offen nt
	buffer_load_dwordx2 v[98:99], v3, s[4:7], s43 offen nt
	buffer_load_dwordx2 v[100:101], v3, s[4:7], s44 offen nt
	buffer_load_dwordx2 v[102:103], v3, s[4:7], s45 offen nt
	buffer_load_dwordx2 v[104:105], v3, s[4:7], s46 offen nt
	buffer_load_dwordx2 v[106:107], v3, s[4:7], s47 offen nt
	buffer_load_dwordx2 v[252:253], v11, s[28:31], 0 offen
	s_mov_b32 s40, 0x0
	s_mov_b32 s41, 0x400
	s_mov_b32 s42, 0x800
	s_mov_b32 s43, 0xc00
	buffer_load_dwordx4 v[108:111], v4, s[8:11], s40 offen
	buffer_load_dwordx4 v[112:115], v4, s[8:11], s41 offen
	buffer_load_dwordx4 v[116:119], v4, s[8:11], s42 offen
	buffer_load_dwordx4 v[120:123], v4, s[8:11], s43 offen
	s_mov_b32 s40, 0x1000
	s_mov_b32 s41, 0x1400
	s_mov_b32 s42, 0x1800
	s_mov_b32 s43, 0x1c00
	buffer_load_dwordx4 v[124:127], v4, s[8:11], s40 offen
	buffer_load_dwordx4 v[128:131], v4, s[8:11], s41 offen
	buffer_load_dwordx4 v[132:135], v4, s[8:11], s42 offen
	buffer_load_dwordx4 v[136:139], v4, s[8:11], s43 offen
	s_mov_b32 s40, 0x10000
	s_mov_b32 s41, 0x10400
	s_mov_b32 s42, 0x10800
	s_mov_b32 s43, 0x10c00
	buffer_load_dwordx4 v[148:151], v4, s[8:11], s40 offen
	buffer_load_dwordx4 v[152:155], v4, s[8:11], s41 offen
	buffer_load_dwordx4 v[156:159], v4, s[8:11], s42 offen
	buffer_load_dwordx4 v[160:163], v4, s[8:11], s43 offen
	s_mov_b32 s40, 0x11000
	s_mov_b32 s41, 0x11400
	s_mov_b32 s42, 0x11800
	s_mov_b32 s43, 0x11c00
	buffer_load_dwordx4 v[164:167], v4, s[8:11], s40 offen
	buffer_load_dwordx4 v[168:171], v4, s[8:11], s41 offen
	buffer_load_dwordx4 v[172:175], v4, s[8:11], s42 offen
	buffer_load_dwordx4 v[176:179], v4, s[8:11], s43 offen
	s_waitcnt vmcnt(41)
	v_cvt_pkrtz_f16_f32 v12, v44, v46
	v_cvt_pkrtz_f16_f32 v13, v48, v50
	v_cvt_pkrtz_f16_f32 v14, v52, v54
	v_cvt_pkrtz_f16_f32 v15, v56, v58
	v_cvt_pkrtz_f16_f32 v16, v45, v47
	v_cvt_pkrtz_f16_f32 v17, v49, v51
	v_cvt_pkrtz_f16_f32 v18, v53, v55
	v_cvt_pkrtz_f16_f32 v19, v57, v59
	s_mov_b32 s40, 0x3c10
	s_mov_b32 s41, 0x258a0
	s_mov_b32 s42, 0x47530
	s_mov_b32 s43, 0x691c0
	s_mov_b32 s44, 0x8ae50
	s_mov_b32 s45, 0xacae0
	s_mov_b32 s46, 0xce770
	s_mov_b32 s47, 0xf0400
	buffer_load_dwordx2 v[44:45], v3, s[4:7], s40 offen nt
	buffer_load_dwordx2 v[46:47], v3, s[4:7], s41 offen nt
	buffer_load_dwordx2 v[48:49], v3, s[4:7], s42 offen nt
	buffer_load_dwordx2 v[50:51], v3, s[4:7], s43 offen nt
	buffer_load_dwordx2 v[52:53], v3, s[4:7], s44 offen nt
	buffer_load_dwordx2 v[54:55], v3, s[4:7], s45 offen nt
	buffer_load_dwordx2 v[56:57], v3, s[4:7], s46 offen nt
	buffer_load_dwordx2 v[58:59], v3, s[4:7], s47 offen nt
	ds_write_b128 v5, v[12:15] offset:0
	ds_write_b128 v5, v[16:19] offset:2048
	s_waitcnt vmcnt(41)
	v_cvt_pkrtz_f16_f32 v12, v60, v62
	v_cvt_pkrtz_f16_f32 v13, v64, v66
	v_cvt_pkrtz_f16_f32 v14, v68, v70
	v_cvt_pkrtz_f16_f32 v15, v72, v74
	v_cvt_pkrtz_f16_f32 v16, v61, v63
	v_cvt_pkrtz_f16_f32 v17, v65, v67
	v_cvt_pkrtz_f16_f32 v18, v69, v71
	v_cvt_pkrtz_f16_f32 v19, v73, v75
	s_mov_b32 s40, 0x112090
	s_mov_b32 s41, 0x133d20
	s_mov_b32 s42, 0x1559b0
	s_mov_b32 s43, 0x177640
	s_mov_b32 s44, 0x1992d0
	s_mov_b32 s45, 0x1baf60
	s_mov_b32 s46, 0x1dcbf0
	s_mov_b32 s47, 0x1fe880
	buffer_load_dwordx2 v[60:61], v3, s[4:7], s40 offen nt
	buffer_load_dwordx2 v[62:63], v3, s[4:7], s41 offen nt
	buffer_load_dwordx2 v[64:65], v3, s[4:7], s42 offen nt
	buffer_load_dwordx2 v[66:67], v3, s[4:7], s43 offen nt
	buffer_load_dwordx2 v[68:69], v3, s[4:7], s44 offen nt
	buffer_load_dwordx2 v[70:71], v3, s[4:7], s45 offen nt
	buffer_load_dwordx2 v[72:73], v3, s[4:7], s46 offen nt
	buffer_load_dwordx2 v[74:75], v3, s[4:7], s47 offen nt
	ds_write_b128 v5, v[12:15] offset:256
	ds_write_b128 v5, v[16:19] offset:2304
	s_waitcnt vmcnt(41)
	v_cvt_pkrtz_f16_f32 v12, v76, v78
	v_cvt_pkrtz_f16_f32 v13, v80, v82
	v_cvt_pkrtz_f16_f32 v14, v84, v86
	v_cvt_pkrtz_f16_f32 v15, v88, v90
	v_cvt_pkrtz_f16_f32 v16, v77, v79
	v_cvt_pkrtz_f16_f32 v17, v81, v83
	v_cvt_pkrtz_f16_f32 v18, v85, v87
	v_cvt_pkrtz_f16_f32 v19, v89, v91
	s_mov_b32 s40, 0x220510
	s_mov_b32 s41, 0x2421a0
	s_mov_b32 s42, 0x263e30
	s_mov_b32 s43, 0x285ac0
	s_mov_b32 s44, 0x2a7750
	s_mov_b32 s45, 0x2c93e0
	s_mov_b32 s46, 0x2eb070
	s_mov_b32 s47, 0x30cd00
	buffer_load_dwordx2 v[76:77], v3, s[4:7], s40 offen nt
	buffer_load_dwordx2 v[78:79], v3, s[4:7], s41 offen nt
	buffer_load_dwordx2 v[80:81], v3, s[4:7], s42 offen nt
	buffer_load_dwordx2 v[82:83], v3, s[4:7], s43 offen nt
	buffer_load_dwordx2 v[84:85], v3, s[4:7], s44 offen nt
	buffer_load_dwordx2 v[86:87], v3, s[4:7], s45 offen nt
	buffer_load_dwordx2 v[88:89], v3, s[4:7], s46 offen nt
	buffer_load_dwordx2 v[90:91], v3, s[4:7], s47 offen nt
	ds_write_b128 v5, v[12:15] offset:512
	ds_write_b128 v5, v[16:19] offset:2560
	s_waitcnt vmcnt(41)
	v_cvt_pkrtz_f16_f32 v12, v92, v94
	v_cvt_pkrtz_f16_f32 v13, v96, v98
	v_cvt_pkrtz_f16_f32 v14, v100, v102
	v_cvt_pkrtz_f16_f32 v15, v104, v106
	v_cvt_pkrtz_f16_f32 v16, v93, v95
	v_cvt_pkrtz_f16_f32 v17, v97, v99
	v_cvt_pkrtz_f16_f32 v18, v101, v103
	v_cvt_pkrtz_f16_f32 v19, v105, v107
	s_mov_b32 s40, 0x32e990
	s_mov_b32 s41, 0x350620
	s_mov_b32 s42, 0x3722b0
	s_mov_b32 s43, 0x393f40
	s_mov_b32 s44, 0x3b5bd0
	s_mov_b32 s45, 0x3d7860
	s_mov_b32 s46, 0x3f94f0
	s_mov_b32 s47, 0x41b180
	buffer_load_dwordx2 v[92:93], v3, s[4:7], s40 offen nt
	buffer_load_dwordx2 v[94:95], v3, s[4:7], s41 offen nt
	buffer_load_dwordx2 v[96:97], v3, s[4:7], s42 offen nt
	buffer_load_dwordx2 v[98:99], v3, s[4:7], s43 offen nt
	buffer_load_dwordx2 v[100:101], v3, s[4:7], s44 offen nt
	buffer_load_dwordx2 v[102:103], v3, s[4:7], s45 offen nt
	buffer_load_dwordx2 v[104:105], v3, s[4:7], s46 offen nt
	buffer_load_dwordx2 v[106:107], v3, s[4:7], s47 offen nt
	ds_write_b128 v5, v[12:15] offset:768
	ds_write_b128 v5, v[16:19] offset:2816
	s_waitcnt lgkmcnt(0)
	s_barrier
	s_waitcnt vmcnt(32)
	ds_write_b128 v254, v[108:111] offset:0
	ds_write_b128 v254, v[112:115] offset:1024
	ds_write_b128 v254, v[148:151] offset:16384
	ds_write_b128 v254, v[152:155] offset:17408
	s_waitcnt lgkmcnt(0)
	s_barrier
	ds_read_b128 v[140:143], v255 offset:0
	ds_read_b128 v[144:147], v255 offset:1024
	ds_read_b128 v[180:183], v255 offset:16384
	ds_read_b128 v[184:187], v255 offset:17408
	ds_read_b128 v[12:15], v6 offset:0
	ds_read_b128 v[16:19], v6 offset:2048
	ds_read_b128 v[20:23], v7 offset:0
	ds_read_b128 v[24:27], v7 offset:2048
	ds_read_b128 v[28:31], v8 offset:0
	ds_read_b128 v[32:35], v8 offset:2048
	ds_read_b128 v[36:39], v9 offset:0
	ds_read_b128 v[40:43], v9 offset:2048
	s_waitcnt lgkmcnt(7)
	v_mfma_f32_16x16x32_f16 v[188:191], v[108:111], v[12:15], 0
	v_mfma_f32_16x16x32_f16 v[220:223], v[148:151], v[12:15], 0
	s_waitcnt lgkmcnt(6)
	v_mfma_f32_16x16x32_f16 v[192:195], v[112:115], v[16:19], 0
	v_mfma_f32_16x16x32_f16 v[224:227], v[152:155], v[16:19], 0
	s_waitcnt lgkmcnt(5)
	v_mfma_f32_16x16x32_f16 v[196:199], v[116:119], v[20:23], 0
	v_mfma_f32_16x16x32_f16 v[228:231], v[156:159], v[20:23], 0
	s_waitcnt lgkmcnt(4)
	v_mfma_f32_16x16x32_f16 v[200:203], v[120:123], v[24:27], 0
	v_mfma_f32_16x16x32_f16 v[232:235], v[160:163], v[24:27], 0
	s_waitcnt lgkmcnt(3)
	v_mfma_f32_16x16x32_f16 v[204:207], v[124:127], v[28:31], 0
	v_mfma_f32_16x16x32_f16 v[236:239], v[164:167], v[28:31], 0
	s_waitcnt lgkmcnt(2)
	v_mfma_f32_16x16x32_f16 v[208:211], v[128:131], v[32:35], 0
	v_mfma_f32_16x16x32_f16 v[240:243], v[168:171], v[32:35], 0
	s_waitcnt lgkmcnt(1)
	v_mfma_f32_16x16x32_f16 v[212:215], v[132:135], v[36:39], 0
	v_mfma_f32_16x16x32_f16 v[244:247], v[172:175], v[36:39], 0
	s_waitcnt lgkmcnt(0)
	v_mfma_f32_16x16x32_f16 v[216:219], v[136:139], v[40:43], 0
	v_mfma_f32_16x16x32_f16 v[248:251], v[176:179], v[40:43], 0
	s_waitcnt vmcnt(24)
	v_cvt_pkrtz_f16_f32 v12, v44, v46
	v_cvt_pkrtz_f16_f32 v13, v48, v50
	v_cvt_pkrtz_f16_f32 v14, v52, v54
	v_cvt_pkrtz_f16_f32 v15, v56, v58
	v_cvt_pkrtz_f16_f32 v16, v45, v47
	v_cvt_pkrtz_f16_f32 v17, v49, v51
	v_cvt_pkrtz_f16_f32 v18, v53, v55
	v_cvt_pkrtz_f16_f32 v19, v57, v59
	s_mov_b32 s40, 0x7820
	s_mov_b32 s41, 0x294b0
	s_mov_b32 s42, 0x4b140
	s_mov_b32 s43, 0x6cdd0
	s_mov_b32 s44, 0x8ea60
	s_mov_b32 s45, 0xb06f0
	s_mov_b32 s46, 0xd2380
	s_mov_b32 s47, 0xf4010
	buffer_load_dwordx2 v[44:45], v3, s[4:7], s40 offen nt
	buffer_load_dwordx2 v[46:47], v3, s[4:7], s41 offen nt
	buffer_load_dwordx2 v[48:49], v3, s[4:7], s42 offen nt
	buffer_load_dwordx2 v[50:51], v3, s[4:7], s43 offen nt
	buffer_load_dwordx2 v[52:53], v3, s[4:7], s44 offen nt
	buffer_load_dwordx2 v[54:55], v3, s[4:7], s45 offen nt
	buffer_load_dwordx2 v[56:57], v3, s[4:7], s46 offen nt
	buffer_load_dwordx2 v[58:59], v3, s[4:7], s47 offen nt
	ds_write_b128 v5, v[12:15] offset:1024
	ds_write_b128 v5, v[16:19] offset:3072
	s_waitcnt vmcnt(24)
	v_cvt_pkrtz_f16_f32 v12, v60, v62
	v_cvt_pkrtz_f16_f32 v13, v64, v66
	v_cvt_pkrtz_f16_f32 v14, v68, v70
	v_cvt_pkrtz_f16_f32 v15, v72, v74
	v_cvt_pkrtz_f16_f32 v16, v61, v63
	v_cvt_pkrtz_f16_f32 v17, v65, v67
	v_cvt_pkrtz_f16_f32 v18, v69, v71
	v_cvt_pkrtz_f16_f32 v19, v73, v75
	s_mov_b32 s40, 0x115ca0
	s_mov_b32 s41, 0x137930
	s_mov_b32 s42, 0x1595c0
	s_mov_b32 s43, 0x17b250
	s_mov_b32 s44, 0x19cee0
	s_mov_b32 s45, 0x1beb70
	s_mov_b32 s46, 0x1e0800
	s_mov_b32 s47, 0x202490
	buffer_load_dwordx2 v[60:61], v3, s[4:7], s40 offen nt
	buffer_load_dwordx2 v[62:63], v3, s[4:7], s41 offen nt
	buffer_load_dwordx2 v[64:65], v3, s[4:7], s42 offen nt
	buffer_load_dwordx2 v[66:67], v3, s[4:7], s43 offen nt
	buffer_load_dwordx2 v[68:69], v3, s[4:7], s44 offen nt
	buffer_load_dwordx2 v[70:71], v3, s[4:7], s45 offen nt
	buffer_load_dwordx2 v[72:73], v3, s[4:7], s46 offen nt
	buffer_load_dwordx2 v[74:75], v3, s[4:7], s47 offen nt
	ds_write_b128 v5, v[12:15] offset:1280
	ds_write_b128 v5, v[16:19] offset:3328
	s_waitcnt vmcnt(24)
	v_cvt_pkrtz_f16_f32 v12, v76, v78
	v_cvt_pkrtz_f16_f32 v13, v80, v82
	v_cvt_pkrtz_f16_f32 v14, v84, v86
	v_cvt_pkrtz_f16_f32 v15, v88, v90
	v_cvt_pkrtz_f16_f32 v16, v77, v79
	v_cvt_pkrtz_f16_f32 v17, v81, v83
	v_cvt_pkrtz_f16_f32 v18, v85, v87
	v_cvt_pkrtz_f16_f32 v19, v89, v91
	s_mov_b32 s40, 0x224120
	s_mov_b32 s41, 0x245db0
	s_mov_b32 s42, 0x267a40
	s_mov_b32 s43, 0x2896d0
	s_mov_b32 s44, 0x2ab360
	s_mov_b32 s45, 0x2ccff0
	s_mov_b32 s46, 0x2eec80
	s_mov_b32 s47, 0x310910
	buffer_load_dwordx2 v[76:77], v3, s[4:7], s40 offen nt
	buffer_load_dwordx2 v[78:79], v3, s[4:7], s41 offen nt
	buffer_load_dwordx2 v[80:81], v3, s[4:7], s42 offen nt
	buffer_load_dwordx2 v[82:83], v3, s[4:7], s43 offen nt
	buffer_load_dwordx2 v[84:85], v3, s[4:7], s44 offen nt
	buffer_load_dwordx2 v[86:87], v3, s[4:7], s45 offen nt
	buffer_load_dwordx2 v[88:89], v3, s[4:7], s46 offen nt
	buffer_load_dwordx2 v[90:91], v3, s[4:7], s47 offen nt
	ds_write_b128 v5, v[12:15] offset:1536
	ds_write_b128 v5, v[16:19] offset:3584
	s_waitcnt vmcnt(24)
	v_cvt_pkrtz_f16_f32 v12, v92, v94
	v_cvt_pkrtz_f16_f32 v13, v96, v98
	v_cvt_pkrtz_f16_f32 v14, v100, v102
	v_cvt_pkrtz_f16_f32 v15, v104, v106
	v_cvt_pkrtz_f16_f32 v16, v93, v95
	v_cvt_pkrtz_f16_f32 v17, v97, v99
	v_cvt_pkrtz_f16_f32 v18, v101, v103
	v_cvt_pkrtz_f16_f32 v19, v105, v107
	s_mov_b32 s40, 0x3325a0
	s_mov_b32 s41, 0x354230
	s_mov_b32 s42, 0x375ec0
	s_mov_b32 s43, 0x397b50
	s_mov_b32 s44, 0x3b97e0
	s_mov_b32 s45, 0x3db470
	s_mov_b32 s46, 0x3fd100
	s_mov_b32 s47, 0x41ed90
	buffer_load_dwordx2 v[92:93], v3, s[4:7], s40 offen nt
	buffer_load_dwordx2 v[94:95], v3, s[4:7], s41 offen nt
	buffer_load_dwordx2 v[96:97], v3, s[4:7], s42 offen nt
	buffer_load_dwordx2 v[98:99], v3, s[4:7], s43 offen nt
	buffer_load_dwordx2 v[100:101], v3, s[4:7], s44 offen nt
	buffer_load_dwordx2 v[102:103], v3, s[4:7], s45 offen nt
	buffer_load_dwordx2 v[104:105], v3, s[4:7], s46 offen nt
	buffer_load_dwordx2 v[106:107], v3, s[4:7], s47 offen nt
	ds_write_b128 v5, v[12:15] offset:1792
	ds_write_b128 v5, v[16:19] offset:3840
	s_waitcnt lgkmcnt(0)
	s_barrier
	ds_read_b128 v[12:15], v6 offset:1024
	ds_read_b128 v[16:19], v6 offset:3072
	ds_read_b128 v[20:23], v7 offset:1024
	ds_read_b128 v[24:27], v7 offset:3072
	ds_read_b128 v[28:31], v8 offset:1024
	ds_read_b128 v[32:35], v8 offset:3072
	ds_read_b128 v[36:39], v9 offset:1024
	ds_read_b128 v[40:43], v9 offset:3072
	s_waitcnt lgkmcnt(7)
	v_mfma_f32_16x16x32_f16 v[188:191], v[112:115], v[12:15], v[188:191]
	v_mfma_f32_16x16x32_f16 v[220:223], v[152:155], v[12:15], v[220:223]
	s_waitcnt lgkmcnt(6)
	v_mfma_f32_16x16x32_f16 v[192:195], v[116:119], v[16:19], v[192:195]
	v_mfma_f32_16x16x32_f16 v[224:227], v[156:159], v[16:19], v[224:227]
	s_waitcnt lgkmcnt(5)
	v_mfma_f32_16x16x32_f16 v[196:199], v[120:123], v[20:23], v[196:199]
	v_mfma_f32_16x16x32_f16 v[228:231], v[160:163], v[20:23], v[228:231]
	s_waitcnt lgkmcnt(4)
	v_mfma_f32_16x16x32_f16 v[200:203], v[124:127], v[24:27], v[200:203]
	v_mfma_f32_16x16x32_f16 v[232:235], v[164:167], v[24:27], v[232:235]
	s_waitcnt lgkmcnt(3)
	v_mfma_f32_16x16x32_f16 v[204:207], v[128:131], v[28:31], v[204:207]
	v_mfma_f32_16x16x32_f16 v[236:239], v[168:171], v[28:31], v[236:239]
	s_waitcnt lgkmcnt(2)
	v_mfma_f32_16x16x32_f16 v[208:211], v[132:135], v[32:35], v[208:211]
	v_mfma_f32_16x16x32_f16 v[240:243], v[172:175], v[32:35], v[240:243]
	s_waitcnt lgkmcnt(1)
	v_mfma_f32_16x16x32_f16 v[212:215], v[136:139], v[36:39], v[212:215]
	v_mfma_f32_16x16x32_f16 v[244:247], v[176:179], v[36:39], v[244:247]
	s_waitcnt lgkmcnt(0)
	v_mfma_f32_16x16x32_f16 v[216:219], v[140:143], v[40:43], v[216:219]
	v_mfma_f32_16x16x32_f16 v[248:251], v[180:183], v[40:43], v[248:251]
	s_waitcnt vmcnt(24)
	v_cvt_pkrtz_f16_f32 v12, v44, v46
	v_cvt_pkrtz_f16_f32 v13, v48, v50
	v_cvt_pkrtz_f16_f32 v14, v52, v54
	v_cvt_pkrtz_f16_f32 v15, v56, v58
	v_cvt_pkrtz_f16_f32 v16, v45, v47
	v_cvt_pkrtz_f16_f32 v17, v49, v51
	v_cvt_pkrtz_f16_f32 v18, v53, v55
	v_cvt_pkrtz_f16_f32 v19, v57, v59
	s_mov_b32 s40, 0xb430
	s_mov_b32 s41, 0x2d0c0
	s_mov_b32 s42, 0x4ed50
	s_mov_b32 s43, 0x709e0
	s_mov_b32 s44, 0x92670
	s_mov_b32 s45, 0xb4300
	s_mov_b32 s46, 0xd5f90
	s_mov_b32 s47, 0xf7c20
	buffer_load_dwordx2 v[44:45], v3, s[4:7], s40 offen nt
	buffer_load_dwordx2 v[46:47], v3, s[4:7], s41 offen nt
	buffer_load_dwordx2 v[48:49], v3, s[4:7], s42 offen nt
	buffer_load_dwordx2 v[50:51], v3, s[4:7], s43 offen nt
	buffer_load_dwordx2 v[52:53], v3, s[4:7], s44 offen nt
	buffer_load_dwordx2 v[54:55], v3, s[4:7], s45 offen nt
	buffer_load_dwordx2 v[56:57], v3, s[4:7], s46 offen nt
	buffer_load_dwordx2 v[58:59], v3, s[4:7], s47 offen nt
	ds_write_b128 v5, v[12:15] offset:0
	ds_write_b128 v5, v[16:19] offset:2048
	s_waitcnt vmcnt(24)
	v_cvt_pkrtz_f16_f32 v12, v60, v62
	v_cvt_pkrtz_f16_f32 v13, v64, v66
	v_cvt_pkrtz_f16_f32 v14, v68, v70
	v_cvt_pkrtz_f16_f32 v15, v72, v74
	v_cvt_pkrtz_f16_f32 v16, v61, v63
	v_cvt_pkrtz_f16_f32 v17, v65, v67
	v_cvt_pkrtz_f16_f32 v18, v69, v71
	v_cvt_pkrtz_f16_f32 v19, v73, v75
	s_mov_b32 s40, 0x1198b0
	s_mov_b32 s41, 0x13b540
	s_mov_b32 s42, 0x15d1d0
	s_mov_b32 s43, 0x17ee60
	s_mov_b32 s44, 0x1a0af0
	s_mov_b32 s45, 0x1c2780
	s_mov_b32 s46, 0x1e4410
	s_mov_b32 s47, 0x2060a0
	buffer_load_dwordx2 v[60:61], v3, s[4:7], s40 offen nt
	buffer_load_dwordx2 v[62:63], v3, s[4:7], s41 offen nt
	buffer_load_dwordx2 v[64:65], v3, s[4:7], s42 offen nt
	buffer_load_dwordx2 v[66:67], v3, s[4:7], s43 offen nt
	buffer_load_dwordx2 v[68:69], v3, s[4:7], s44 offen nt
	buffer_load_dwordx2 v[70:71], v3, s[4:7], s45 offen nt
	buffer_load_dwordx2 v[72:73], v3, s[4:7], s46 offen nt
	buffer_load_dwordx2 v[74:75], v3, s[4:7], s47 offen nt
	ds_write_b128 v5, v[12:15] offset:256
	ds_write_b128 v5, v[16:19] offset:2304
	s_waitcnt vmcnt(24)
	v_cvt_pkrtz_f16_f32 v12, v76, v78
	v_cvt_pkrtz_f16_f32 v13, v80, v82
	v_cvt_pkrtz_f16_f32 v14, v84, v86
	v_cvt_pkrtz_f16_f32 v15, v88, v90
	v_cvt_pkrtz_f16_f32 v16, v77, v79
	v_cvt_pkrtz_f16_f32 v17, v81, v83
	v_cvt_pkrtz_f16_f32 v18, v85, v87
	v_cvt_pkrtz_f16_f32 v19, v89, v91
	s_mov_b32 s40, 0x227d30
	s_mov_b32 s41, 0x2499c0
	s_mov_b32 s42, 0x26b650
	s_mov_b32 s43, 0x28d2e0
	s_mov_b32 s44, 0x2aef70
	s_mov_b32 s45, 0x2d0c00
	s_mov_b32 s46, 0x2f2890
	s_mov_b32 s47, 0x314520
	buffer_load_dwordx2 v[76:77], v3, s[4:7], s40 offen nt
	buffer_load_dwordx2 v[78:79], v3, s[4:7], s41 offen nt
	buffer_load_dwordx2 v[80:81], v3, s[4:7], s42 offen nt
	buffer_load_dwordx2 v[82:83], v3, s[4:7], s43 offen nt
	buffer_load_dwordx2 v[84:85], v3, s[4:7], s44 offen nt
	buffer_load_dwordx2 v[86:87], v3, s[4:7], s45 offen nt
	buffer_load_dwordx2 v[88:89], v3, s[4:7], s46 offen nt
	buffer_load_dwordx2 v[90:91], v3, s[4:7], s47 offen nt
	ds_write_b128 v5, v[12:15] offset:512
	ds_write_b128 v5, v[16:19] offset:2560
	s_waitcnt vmcnt(24)
	v_cvt_pkrtz_f16_f32 v12, v92, v94
	v_cvt_pkrtz_f16_f32 v13, v96, v98
	v_cvt_pkrtz_f16_f32 v14, v100, v102
	v_cvt_pkrtz_f16_f32 v15, v104, v106
	v_cvt_pkrtz_f16_f32 v16, v93, v95
	v_cvt_pkrtz_f16_f32 v17, v97, v99
	v_cvt_pkrtz_f16_f32 v18, v101, v103
	v_cvt_pkrtz_f16_f32 v19, v105, v107
	s_mov_b32 s40, 0x3361b0
	s_mov_b32 s41, 0x357e40
	s_mov_b32 s42, 0x379ad0
	s_mov_b32 s43, 0x39b760
	s_mov_b32 s44, 0x3bd3f0
	s_mov_b32 s45, 0x3df080
	s_mov_b32 s46, 0x400d10
	s_mov_b32 s47, 0x4229a0
	buffer_load_dwordx2 v[92:93], v3, s[4:7], s40 offen nt
	buffer_load_dwordx2 v[94:95], v3, s[4:7], s41 offen nt
	buffer_load_dwordx2 v[96:97], v3, s[4:7], s42 offen nt
	buffer_load_dwordx2 v[98:99], v3, s[4:7], s43 offen nt
	buffer_load_dwordx2 v[100:101], v3, s[4:7], s44 offen nt
	buffer_load_dwordx2 v[102:103], v3, s[4:7], s45 offen nt
	buffer_load_dwordx2 v[104:105], v3, s[4:7], s46 offen nt
	buffer_load_dwordx2 v[106:107], v3, s[4:7], s47 offen nt
	ds_write_b128 v5, v[12:15] offset:768
	ds_write_b128 v5, v[16:19] offset:2816
	s_waitcnt lgkmcnt(0)
	s_barrier
	ds_read_b128 v[12:15], v6 offset:0
	ds_read_b128 v[16:19], v6 offset:2048
	ds_read_b128 v[20:23], v7 offset:0
	ds_read_b128 v[24:27], v7 offset:2048
	ds_read_b128 v[28:31], v8 offset:0
	ds_read_b128 v[32:35], v8 offset:2048
	ds_read_b128 v[36:39], v9 offset:0
	ds_read_b128 v[40:43], v9 offset:2048
	s_waitcnt lgkmcnt(7)
	v_mfma_f32_16x16x32_f16 v[188:191], v[116:119], v[12:15], v[188:191]
	v_mfma_f32_16x16x32_f16 v[220:223], v[156:159], v[12:15], v[220:223]
	s_waitcnt lgkmcnt(6)
	v_mfma_f32_16x16x32_f16 v[192:195], v[120:123], v[16:19], v[192:195]
	v_mfma_f32_16x16x32_f16 v[224:227], v[160:163], v[16:19], v[224:227]
	s_waitcnt lgkmcnt(5)
	v_mfma_f32_16x16x32_f16 v[196:199], v[124:127], v[20:23], v[196:199]
	v_mfma_f32_16x16x32_f16 v[228:231], v[164:167], v[20:23], v[228:231]
	s_waitcnt lgkmcnt(4)
	v_mfma_f32_16x16x32_f16 v[200:203], v[128:131], v[24:27], v[200:203]
	v_mfma_f32_16x16x32_f16 v[232:235], v[168:171], v[24:27], v[232:235]
	s_waitcnt lgkmcnt(3)
	v_mfma_f32_16x16x32_f16 v[204:207], v[132:135], v[28:31], v[204:207]
	v_mfma_f32_16x16x32_f16 v[236:239], v[172:175], v[28:31], v[236:239]
	s_waitcnt lgkmcnt(2)
	v_mfma_f32_16x16x32_f16 v[208:211], v[136:139], v[32:35], v[208:211]
	v_mfma_f32_16x16x32_f16 v[240:243], v[176:179], v[32:35], v[240:243]
	s_waitcnt lgkmcnt(1)
	v_mfma_f32_16x16x32_f16 v[212:215], v[140:143], v[36:39], v[212:215]
	v_mfma_f32_16x16x32_f16 v[244:247], v[180:183], v[36:39], v[244:247]
	s_waitcnt lgkmcnt(0)
	v_mfma_f32_16x16x32_f16 v[216:219], v[144:147], v[40:43], v[216:219]
	v_mfma_f32_16x16x32_f16 v[248:251], v[184:187], v[40:43], v[248:251]
	s_mov_b32 s40, 0x20000
	s_mov_b32 s41, 0x20400
	s_mov_b32 s42, 0x20800
	s_mov_b32 s43, 0x20c00
	buffer_load_dwordx4 v[108:111], v4, s[8:11], s40 offen
	buffer_load_dwordx4 v[112:115], v4, s[8:11], s41 offen
	buffer_load_dwordx4 v[116:119], v4, s[8:11], s42 offen
	buffer_load_dwordx4 v[120:123], v4, s[8:11], s43 offen
	s_mov_b32 s40, 0x21000
	s_mov_b32 s41, 0x21400
	s_mov_b32 s42, 0x21800
	s_mov_b32 s43, 0x21c00
	buffer_load_dwordx4 v[124:127], v4, s[8:11], s40 offen
	buffer_load_dwordx4 v[128:131], v4, s[8:11], s41 offen
	buffer_load_dwordx4 v[132:135], v4, s[8:11], s42 offen
	buffer_load_dwordx4 v[136:139], v4, s[8:11], s43 offen
	s_waitcnt vmcnt(32)
	v_cvt_pkrtz_f16_f32 v12, v44, v46
	v_cvt_pkrtz_f16_f32 v13, v48, v50
	v_cvt_pkrtz_f16_f32 v14, v52, v54
	v_cvt_pkrtz_f16_f32 v15, v56, v58
	v_cvt_pkrtz_f16_f32 v16, v45, v47
	v_cvt_pkrtz_f16_f32 v17, v49, v51
	v_cvt_pkrtz_f16_f32 v18, v53, v55
	v_cvt_pkrtz_f16_f32 v19, v57, v59
	s_mov_b32 s40, 0xf040
	s_mov_b32 s41, 0x30cd0
	s_mov_b32 s42, 0x52960
	s_mov_b32 s43, 0x745f0
	s_mov_b32 s44, 0x96280
	s_mov_b32 s45, 0xb7f10
	s_mov_b32 s46, 0xd9ba0
	s_mov_b32 s47, 0xfb830
	buffer_load_dwordx2 v[44:45], v3, s[4:7], s40 offen nt
	buffer_load_dwordx2 v[46:47], v3, s[4:7], s41 offen nt
	buffer_load_dwordx2 v[48:49], v3, s[4:7], s42 offen nt
	buffer_load_dwordx2 v[50:51], v3, s[4:7], s43 offen nt
	buffer_load_dwordx2 v[52:53], v3, s[4:7], s44 offen nt
	buffer_load_dwordx2 v[54:55], v3, s[4:7], s45 offen nt
	buffer_load_dwordx2 v[56:57], v3, s[4:7], s46 offen nt
	buffer_load_dwordx2 v[58:59], v3, s[4:7], s47 offen nt
	ds_write_b128 v5, v[12:15] offset:1024
	ds_write_b128 v5, v[16:19] offset:3072
	s_waitcnt vmcnt(32)
	v_cvt_pkrtz_f16_f32 v12, v60, v62
	v_cvt_pkrtz_f16_f32 v13, v64, v66
	v_cvt_pkrtz_f16_f32 v14, v68, v70
	v_cvt_pkrtz_f16_f32 v15, v72, v74
	v_cvt_pkrtz_f16_f32 v16, v61, v63
	v_cvt_pkrtz_f16_f32 v17, v65, v67
	v_cvt_pkrtz_f16_f32 v18, v69, v71
	v_cvt_pkrtz_f16_f32 v19, v73, v75
	s_mov_b32 s40, 0x11d4c0
	s_mov_b32 s41, 0x13f150
	s_mov_b32 s42, 0x160de0
	s_mov_b32 s43, 0x182a70
	s_mov_b32 s44, 0x1a4700
	s_mov_b32 s45, 0x1c6390
	s_mov_b32 s46, 0x1e8020
	s_mov_b32 s47, 0x209cb0
	buffer_load_dwordx2 v[60:61], v3, s[4:7], s40 offen nt
	buffer_load_dwordx2 v[62:63], v3, s[4:7], s41 offen nt
	buffer_load_dwordx2 v[64:65], v3, s[4:7], s42 offen nt
	buffer_load_dwordx2 v[66:67], v3, s[4:7], s43 offen nt
	buffer_load_dwordx2 v[68:69], v3, s[4:7], s44 offen nt
	buffer_load_dwordx2 v[70:71], v3, s[4:7], s45 offen nt
	buffer_load_dwordx2 v[72:73], v3, s[4:7], s46 offen nt
	buffer_load_dwordx2 v[74:75], v3, s[4:7], s47 offen nt
	ds_write_b128 v5, v[12:15] offset:1280
	ds_write_b128 v5, v[16:19] offset:3328
	s_waitcnt vmcnt(32)
	v_cvt_pkrtz_f16_f32 v12, v76, v78
	v_cvt_pkrtz_f16_f32 v13, v80, v82
	v_cvt_pkrtz_f16_f32 v14, v84, v86
	v_cvt_pkrtz_f16_f32 v15, v88, v90
	v_cvt_pkrtz_f16_f32 v16, v77, v79
	v_cvt_pkrtz_f16_f32 v17, v81, v83
	v_cvt_pkrtz_f16_f32 v18, v85, v87
	v_cvt_pkrtz_f16_f32 v19, v89, v91
	s_mov_b32 s40, 0x22b940
	s_mov_b32 s41, 0x24d5d0
	s_mov_b32 s42, 0x26f260
	s_mov_b32 s43, 0x290ef0
	s_mov_b32 s44, 0x2b2b80
	s_mov_b32 s45, 0x2d4810
	s_mov_b32 s46, 0x2f64a0
	s_mov_b32 s47, 0x318130
	buffer_load_dwordx2 v[76:77], v3, s[4:7], s40 offen nt
	buffer_load_dwordx2 v[78:79], v3, s[4:7], s41 offen nt
	buffer_load_dwordx2 v[80:81], v3, s[4:7], s42 offen nt
	buffer_load_dwordx2 v[82:83], v3, s[4:7], s43 offen nt
	buffer_load_dwordx2 v[84:85], v3, s[4:7], s44 offen nt
	buffer_load_dwordx2 v[86:87], v3, s[4:7], s45 offen nt
	buffer_load_dwordx2 v[88:89], v3, s[4:7], s46 offen nt
	buffer_load_dwordx2 v[90:91], v3, s[4:7], s47 offen nt
	ds_write_b128 v5, v[12:15] offset:1536
	ds_write_b128 v5, v[16:19] offset:3584
	s_waitcnt vmcnt(32)
	v_cvt_pkrtz_f16_f32 v12, v92, v94
	v_cvt_pkrtz_f16_f32 v13, v96, v98
	v_cvt_pkrtz_f16_f32 v14, v100, v102
	v_cvt_pkrtz_f16_f32 v15, v104, v106
	v_cvt_pkrtz_f16_f32 v16, v93, v95
	v_cvt_pkrtz_f16_f32 v17, v97, v99
	v_cvt_pkrtz_f16_f32 v18, v101, v103
	v_cvt_pkrtz_f16_f32 v19, v105, v107
	s_mov_b32 s40, 0x339dc0
	s_mov_b32 s41, 0x35ba50
	s_mov_b32 s42, 0x37d6e0
	s_mov_b32 s43, 0x39f370
	s_mov_b32 s44, 0x3c1000
	s_mov_b32 s45, 0x3e2c90
	s_mov_b32 s46, 0x404920
	s_mov_b32 s47, 0x4265b0
	buffer_load_dwordx2 v[92:93], v3, s[4:7], s40 offen nt
	buffer_load_dwordx2 v[94:95], v3, s[4:7], s41 offen nt
	buffer_load_dwordx2 v[96:97], v3, s[4:7], s42 offen nt
	buffer_load_dwordx2 v[98:99], v3, s[4:7], s43 offen nt
	buffer_load_dwordx2 v[100:101], v3, s[4:7], s44 offen nt
	buffer_load_dwordx2 v[102:103], v3, s[4:7], s45 offen nt
	buffer_load_dwordx2 v[104:105], v3, s[4:7], s46 offen nt
	buffer_load_dwordx2 v[106:107], v3, s[4:7], s47 offen nt
	ds_write_b128 v5, v[12:15] offset:1792
	ds_write_b128 v5, v[16:19] offset:3840
	s_waitcnt lgkmcnt(0)
	s_barrier
	s_waitcnt vmcnt(32)
	ds_write_b128 v254, v[108:111] offset:0
	ds_write_b128 v254, v[112:115] offset:1024
	s_waitcnt lgkmcnt(0)
	s_barrier
	ds_read_b128 v[140:143], v255 offset:0
	ds_read_b128 v[144:147], v255 offset:1024
	ds_read_b128 v[12:15], v6 offset:1024
	ds_read_b128 v[16:19], v6 offset:3072
	ds_read_b128 v[20:23], v7 offset:1024
	ds_read_b128 v[24:27], v7 offset:3072
	ds_read_b128 v[28:31], v8 offset:1024
	ds_read_b128 v[32:35], v8 offset:3072
	ds_read_b128 v[36:39], v9 offset:1024
	ds_read_b128 v[40:43], v9 offset:3072
	s_waitcnt lgkmcnt(7)
	v_mfma_f32_16x16x32_f16 v[188:191], v[148:151], v[12:15], v[188:191]
	v_mfma_f32_16x16x32_f16 v[220:223], v[108:111], v[12:15], v[220:223]
	s_waitcnt lgkmcnt(6)
	v_mfma_f32_16x16x32_f16 v[192:195], v[152:155], v[16:19], v[192:195]
	v_mfma_f32_16x16x32_f16 v[224:227], v[112:115], v[16:19], v[224:227]
	s_waitcnt lgkmcnt(5)
	v_mfma_f32_16x16x32_f16 v[196:199], v[156:159], v[20:23], v[196:199]
	v_mfma_f32_16x16x32_f16 v[228:231], v[116:119], v[20:23], v[228:231]
	s_waitcnt lgkmcnt(4)
	v_mfma_f32_16x16x32_f16 v[200:203], v[160:163], v[24:27], v[200:203]
	v_mfma_f32_16x16x32_f16 v[232:235], v[120:123], v[24:27], v[232:235]
	s_waitcnt lgkmcnt(3)
	v_mfma_f32_16x16x32_f16 v[204:207], v[164:167], v[28:31], v[204:207]
	v_mfma_f32_16x16x32_f16 v[236:239], v[124:127], v[28:31], v[236:239]
	s_waitcnt lgkmcnt(2)
	v_mfma_f32_16x16x32_f16 v[208:211], v[168:171], v[32:35], v[208:211]
	v_mfma_f32_16x16x32_f16 v[240:243], v[128:131], v[32:35], v[240:243]
	s_waitcnt lgkmcnt(1)
	v_mfma_f32_16x16x32_f16 v[212:215], v[172:175], v[36:39], v[212:215]
	v_mfma_f32_16x16x32_f16 v[244:247], v[132:135], v[36:39], v[244:247]
	s_waitcnt lgkmcnt(0)
	v_mfma_f32_16x16x32_f16 v[216:219], v[176:179], v[40:43], v[216:219]
	v_mfma_f32_16x16x32_f16 v[248:251], v[136:139], v[40:43], v[248:251]
	s_waitcnt vmcnt(24)
	v_cvt_pkrtz_f16_f32 v12, v44, v46
	v_cvt_pkrtz_f16_f32 v13, v48, v50
	v_cvt_pkrtz_f16_f32 v14, v52, v54
	v_cvt_pkrtz_f16_f32 v15, v56, v58
	v_cvt_pkrtz_f16_f32 v16, v45, v47
	v_cvt_pkrtz_f16_f32 v17, v49, v51
	v_cvt_pkrtz_f16_f32 v18, v53, v55
	v_cvt_pkrtz_f16_f32 v19, v57, v59
	s_mov_b32 s40, 0x12c50
	s_mov_b32 s41, 0x348e0
	s_mov_b32 s42, 0x56570
	s_mov_b32 s43, 0x78200
	s_mov_b32 s44, 0x99e90
	s_mov_b32 s45, 0xbbb20
	s_mov_b32 s46, 0xdd7b0
	s_mov_b32 s47, 0xff440
	buffer_load_dwordx2 v[44:45], v3, s[4:7], s40 offen nt
	buffer_load_dwordx2 v[46:47], v3, s[4:7], s41 offen nt
	buffer_load_dwordx2 v[48:49], v3, s[4:7], s42 offen nt
	buffer_load_dwordx2 v[50:51], v3, s[4:7], s43 offen nt
	buffer_load_dwordx2 v[52:53], v3, s[4:7], s44 offen nt
	buffer_load_dwordx2 v[54:55], v3, s[4:7], s45 offen nt
	buffer_load_dwordx2 v[56:57], v3, s[4:7], s46 offen nt
	buffer_load_dwordx2 v[58:59], v3, s[4:7], s47 offen nt
	ds_write_b128 v5, v[12:15] offset:0
	ds_write_b128 v5, v[16:19] offset:2048
	s_waitcnt vmcnt(24)
	v_cvt_pkrtz_f16_f32 v12, v60, v62
	v_cvt_pkrtz_f16_f32 v13, v64, v66
	v_cvt_pkrtz_f16_f32 v14, v68, v70
	v_cvt_pkrtz_f16_f32 v15, v72, v74
	v_cvt_pkrtz_f16_f32 v16, v61, v63
	v_cvt_pkrtz_f16_f32 v17, v65, v67
	v_cvt_pkrtz_f16_f32 v18, v69, v71
	v_cvt_pkrtz_f16_f32 v19, v73, v75
	s_mov_b32 s40, 0x1210d0
	s_mov_b32 s41, 0x142d60
	s_mov_b32 s42, 0x1649f0
	s_mov_b32 s43, 0x186680
	s_mov_b32 s44, 0x1a8310
	s_mov_b32 s45, 0x1c9fa0
	s_mov_b32 s46, 0x1ebc30
	s_mov_b32 s47, 0x20d8c0
	buffer_load_dwordx2 v[60:61], v3, s[4:7], s40 offen nt
	buffer_load_dwordx2 v[62:63], v3, s[4:7], s41 offen nt
	buffer_load_dwordx2 v[64:65], v3, s[4:7], s42 offen nt
	buffer_load_dwordx2 v[66:67], v3, s[4:7], s43 offen nt
	buffer_load_dwordx2 v[68:69], v3, s[4:7], s44 offen nt
	buffer_load_dwordx2 v[70:71], v3, s[4:7], s45 offen nt
	buffer_load_dwordx2 v[72:73], v3, s[4:7], s46 offen nt
	buffer_load_dwordx2 v[74:75], v3, s[4:7], s47 offen nt
	ds_write_b128 v5, v[12:15] offset:256
	ds_write_b128 v5, v[16:19] offset:2304
	s_waitcnt vmcnt(24)
	v_cvt_pkrtz_f16_f32 v12, v76, v78
	v_cvt_pkrtz_f16_f32 v13, v80, v82
	v_cvt_pkrtz_f16_f32 v14, v84, v86
	v_cvt_pkrtz_f16_f32 v15, v88, v90
	v_cvt_pkrtz_f16_f32 v16, v77, v79
	v_cvt_pkrtz_f16_f32 v17, v81, v83
	v_cvt_pkrtz_f16_f32 v18, v85, v87
	v_cvt_pkrtz_f16_f32 v19, v89, v91
	s_mov_b32 s40, 0x22f550
	s_mov_b32 s41, 0x2511e0
	s_mov_b32 s42, 0x272e70
	s_mov_b32 s43, 0x294b00
	s_mov_b32 s44, 0x2b6790
	s_mov_b32 s45, 0x2d8420
	s_mov_b32 s46, 0x2fa0b0
	s_mov_b32 s47, 0x31bd40
	buffer_load_dwordx2 v[76:77], v3, s[4:7], s40 offen nt
	buffer_load_dwordx2 v[78:79], v3, s[4:7], s41 offen nt
	buffer_load_dwordx2 v[80:81], v3, s[4:7], s42 offen nt
	buffer_load_dwordx2 v[82:83], v3, s[4:7], s43 offen nt
	buffer_load_dwordx2 v[84:85], v3, s[4:7], s44 offen nt
	buffer_load_dwordx2 v[86:87], v3, s[4:7], s45 offen nt
	buffer_load_dwordx2 v[88:89], v3, s[4:7], s46 offen nt
	buffer_load_dwordx2 v[90:91], v3, s[4:7], s47 offen nt
	ds_write_b128 v5, v[12:15] offset:512
	ds_write_b128 v5, v[16:19] offset:2560
	s_waitcnt vmcnt(24)
	v_cvt_pkrtz_f16_f32 v12, v92, v94
	v_cvt_pkrtz_f16_f32 v13, v96, v98
	v_cvt_pkrtz_f16_f32 v14, v100, v102
	v_cvt_pkrtz_f16_f32 v15, v104, v106
	v_cvt_pkrtz_f16_f32 v16, v93, v95
	v_cvt_pkrtz_f16_f32 v17, v97, v99
	v_cvt_pkrtz_f16_f32 v18, v101, v103
	v_cvt_pkrtz_f16_f32 v19, v105, v107
	s_mov_b32 s40, 0x33d9d0
	s_mov_b32 s41, 0x35f660
	s_mov_b32 s42, 0x3812f0
	s_mov_b32 s43, 0x3a2f80
	s_mov_b32 s44, 0x3c4c10
	s_mov_b32 s45, 0x3e68a0
	s_mov_b32 s46, 0x408530
	s_mov_b32 s47, 0x42a1c0
	buffer_load_dwordx2 v[92:93], v3, s[4:7], s40 offen nt
	buffer_load_dwordx2 v[94:95], v3, s[4:7], s41 offen nt
	buffer_load_dwordx2 v[96:97], v3, s[4:7], s42 offen nt
	buffer_load_dwordx2 v[98:99], v3, s[4:7], s43 offen nt
	buffer_load_dwordx2 v[100:101], v3, s[4:7], s44 offen nt
	buffer_load_dwordx2 v[102:103], v3, s[4:7], s45 offen nt
	buffer_load_dwordx2 v[104:105], v3, s[4:7], s46 offen nt
	buffer_load_dwordx2 v[106:107], v3, s[4:7], s47 offen nt
	ds_write_b128 v5, v[12:15] offset:768
	ds_write_b128 v5, v[16:19] offset:2816
	s_waitcnt lgkmcnt(0)
	s_barrier
	ds_read_b128 v[12:15], v6 offset:0
	ds_read_b128 v[16:19], v6 offset:2048
	ds_read_b128 v[20:23], v7 offset:0
	ds_read_b128 v[24:27], v7 offset:2048
	ds_read_b128 v[28:31], v8 offset:0
	ds_read_b128 v[32:35], v8 offset:2048
	ds_read_b128 v[36:39], v9 offset:0
	ds_read_b128 v[40:43], v9 offset:2048
	s_waitcnt lgkmcnt(7)
	v_mfma_f32_16x16x32_f16 v[188:191], v[152:155], v[12:15], v[188:191]
	v_mfma_f32_16x16x32_f16 v[220:223], v[112:115], v[12:15], v[220:223]
	s_waitcnt lgkmcnt(6)
	v_mfma_f32_16x16x32_f16 v[192:195], v[156:159], v[16:19], v[192:195]
	v_mfma_f32_16x16x32_f16 v[224:227], v[116:119], v[16:19], v[224:227]
	s_waitcnt lgkmcnt(5)
	v_mfma_f32_16x16x32_f16 v[196:199], v[160:163], v[20:23], v[196:199]
	v_mfma_f32_16x16x32_f16 v[228:231], v[120:123], v[20:23], v[228:231]
	s_waitcnt lgkmcnt(4)
	v_mfma_f32_16x16x32_f16 v[200:203], v[164:167], v[24:27], v[200:203]
	v_mfma_f32_16x16x32_f16 v[232:235], v[124:127], v[24:27], v[232:235]
	s_waitcnt lgkmcnt(3)
	v_mfma_f32_16x16x32_f16 v[204:207], v[168:171], v[28:31], v[204:207]
	v_mfma_f32_16x16x32_f16 v[236:239], v[128:131], v[28:31], v[236:239]
	s_waitcnt lgkmcnt(2)
	v_mfma_f32_16x16x32_f16 v[208:211], v[172:175], v[32:35], v[208:211]
	v_mfma_f32_16x16x32_f16 v[240:243], v[132:135], v[32:35], v[240:243]
	s_waitcnt lgkmcnt(1)
	v_mfma_f32_16x16x32_f16 v[212:215], v[176:179], v[36:39], v[212:215]
	v_mfma_f32_16x16x32_f16 v[244:247], v[136:139], v[36:39], v[244:247]
	s_waitcnt lgkmcnt(0)
	v_mfma_f32_16x16x32_f16 v[216:219], v[180:183], v[40:43], v[216:219]
	v_mfma_f32_16x16x32_f16 v[248:251], v[140:143], v[40:43], v[248:251]
	s_waitcnt vmcnt(24)
	v_cvt_pkrtz_f16_f32 v12, v44, v46
	v_cvt_pkrtz_f16_f32 v13, v48, v50
	v_cvt_pkrtz_f16_f32 v14, v52, v54
	v_cvt_pkrtz_f16_f32 v15, v56, v58
	v_cvt_pkrtz_f16_f32 v16, v45, v47
	v_cvt_pkrtz_f16_f32 v17, v49, v51
	v_cvt_pkrtz_f16_f32 v18, v53, v55
	v_cvt_pkrtz_f16_f32 v19, v57, v59
	s_mov_b32 s40, 0x16860
	s_mov_b32 s41, 0x384f0
	s_mov_b32 s42, 0x5a180
	s_mov_b32 s43, 0x7be10
	s_mov_b32 s44, 0x9daa0
	s_mov_b32 s45, 0xbf730
	s_mov_b32 s46, 0xe13c0
	s_mov_b32 s47, 0x103050
	buffer_load_dwordx2 v[44:45], v3, s[4:7], s40 offen nt
	buffer_load_dwordx2 v[46:47], v3, s[4:7], s41 offen nt
	buffer_load_dwordx2 v[48:49], v3, s[4:7], s42 offen nt
	buffer_load_dwordx2 v[50:51], v3, s[4:7], s43 offen nt
	buffer_load_dwordx2 v[52:53], v3, s[4:7], s44 offen nt
	buffer_load_dwordx2 v[54:55], v3, s[4:7], s45 offen nt
	buffer_load_dwordx2 v[56:57], v3, s[4:7], s46 offen nt
	buffer_load_dwordx2 v[58:59], v3, s[4:7], s47 offen nt
	ds_write_b128 v5, v[12:15] offset:1024
	ds_write_b128 v5, v[16:19] offset:3072
	s_waitcnt vmcnt(24)
	v_cvt_pkrtz_f16_f32 v12, v60, v62
	v_cvt_pkrtz_f16_f32 v13, v64, v66
	v_cvt_pkrtz_f16_f32 v14, v68, v70
	v_cvt_pkrtz_f16_f32 v15, v72, v74
	v_cvt_pkrtz_f16_f32 v16, v61, v63
	v_cvt_pkrtz_f16_f32 v17, v65, v67
	v_cvt_pkrtz_f16_f32 v18, v69, v71
	v_cvt_pkrtz_f16_f32 v19, v73, v75
	s_mov_b32 s40, 0x124ce0
	s_mov_b32 s41, 0x146970
	s_mov_b32 s42, 0x168600
	s_mov_b32 s43, 0x18a290
	s_mov_b32 s44, 0x1abf20
	s_mov_b32 s45, 0x1cdbb0
	s_mov_b32 s46, 0x1ef840
	s_mov_b32 s47, 0x2114d0
	buffer_load_dwordx2 v[60:61], v3, s[4:7], s40 offen nt
	buffer_load_dwordx2 v[62:63], v3, s[4:7], s41 offen nt
	buffer_load_dwordx2 v[64:65], v3, s[4:7], s42 offen nt
	buffer_load_dwordx2 v[66:67], v3, s[4:7], s43 offen nt
	buffer_load_dwordx2 v[68:69], v3, s[4:7], s44 offen nt
	buffer_load_dwordx2 v[70:71], v3, s[4:7], s45 offen nt
	buffer_load_dwordx2 v[72:73], v3, s[4:7], s46 offen nt
	buffer_load_dwordx2 v[74:75], v3, s[4:7], s47 offen nt
	ds_write_b128 v5, v[12:15] offset:1280
	ds_write_b128 v5, v[16:19] offset:3328
	s_waitcnt vmcnt(24)
	v_cvt_pkrtz_f16_f32 v12, v76, v78
	v_cvt_pkrtz_f16_f32 v13, v80, v82
	v_cvt_pkrtz_f16_f32 v14, v84, v86
	v_cvt_pkrtz_f16_f32 v15, v88, v90
	v_cvt_pkrtz_f16_f32 v16, v77, v79
	v_cvt_pkrtz_f16_f32 v17, v81, v83
	v_cvt_pkrtz_f16_f32 v18, v85, v87
	v_cvt_pkrtz_f16_f32 v19, v89, v91
	s_mov_b32 s40, 0x233160
	s_mov_b32 s41, 0x254df0
	s_mov_b32 s42, 0x276a80
	s_mov_b32 s43, 0x298710
	s_mov_b32 s44, 0x2ba3a0
	s_mov_b32 s45, 0x2dc030
	s_mov_b32 s46, 0x2fdcc0
	s_mov_b32 s47, 0x31f950
	buffer_load_dwordx2 v[76:77], v3, s[4:7], s40 offen nt
	buffer_load_dwordx2 v[78:79], v3, s[4:7], s41 offen nt
	buffer_load_dwordx2 v[80:81], v3, s[4:7], s42 offen nt
	buffer_load_dwordx2 v[82:83], v3, s[4:7], s43 offen nt
	buffer_load_dwordx2 v[84:85], v3, s[4:7], s44 offen nt
	buffer_load_dwordx2 v[86:87], v3, s[4:7], s45 offen nt
	buffer_load_dwordx2 v[88:89], v3, s[4:7], s46 offen nt
	buffer_load_dwordx2 v[90:91], v3, s[4:7], s47 offen nt
	ds_write_b128 v5, v[12:15] offset:1536
	ds_write_b128 v5, v[16:19] offset:3584
	s_waitcnt vmcnt(24)
	v_cvt_pkrtz_f16_f32 v12, v92, v94
	v_cvt_pkrtz_f16_f32 v13, v96, v98
	v_cvt_pkrtz_f16_f32 v14, v100, v102
	v_cvt_pkrtz_f16_f32 v15, v104, v106
	v_cvt_pkrtz_f16_f32 v16, v93, v95
	v_cvt_pkrtz_f16_f32 v17, v97, v99
	v_cvt_pkrtz_f16_f32 v18, v101, v103
	v_cvt_pkrtz_f16_f32 v19, v105, v107
	s_mov_b32 s40, 0x3415e0
	s_mov_b32 s41, 0x363270
	s_mov_b32 s42, 0x384f00
	s_mov_b32 s43, 0x3a6b90
	s_mov_b32 s44, 0x3c8820
	s_mov_b32 s45, 0x3ea4b0
	s_mov_b32 s46, 0x40c140
	s_mov_b32 s47, 0x42ddd0
	buffer_load_dwordx2 v[92:93], v3, s[4:7], s40 offen nt
	buffer_load_dwordx2 v[94:95], v3, s[4:7], s41 offen nt
	buffer_load_dwordx2 v[96:97], v3, s[4:7], s42 offen nt
	buffer_load_dwordx2 v[98:99], v3, s[4:7], s43 offen nt
	buffer_load_dwordx2 v[100:101], v3, s[4:7], s44 offen nt
	buffer_load_dwordx2 v[102:103], v3, s[4:7], s45 offen nt
	buffer_load_dwordx2 v[104:105], v3, s[4:7], s46 offen nt
	buffer_load_dwordx2 v[106:107], v3, s[4:7], s47 offen nt
	ds_write_b128 v5, v[12:15] offset:1792
	ds_write_b128 v5, v[16:19] offset:3840
	s_waitcnt lgkmcnt(0)
	s_barrier
	ds_read_b128 v[12:15], v6 offset:1024
	ds_read_b128 v[16:19], v6 offset:3072
	ds_read_b128 v[20:23], v7 offset:1024
	ds_read_b128 v[24:27], v7 offset:3072
	ds_read_b128 v[28:31], v8 offset:1024
	ds_read_b128 v[32:35], v8 offset:3072
	ds_read_b128 v[36:39], v9 offset:1024
	ds_read_b128 v[40:43], v9 offset:3072
	s_waitcnt lgkmcnt(7)
	v_mfma_f32_16x16x32_f16 v[188:191], v[156:159], v[12:15], v[188:191]
	v_mfma_f32_16x16x32_f16 v[220:223], v[116:119], v[12:15], v[220:223]
	s_waitcnt lgkmcnt(6)
	v_mfma_f32_16x16x32_f16 v[192:195], v[160:163], v[16:19], v[192:195]
	v_mfma_f32_16x16x32_f16 v[224:227], v[120:123], v[16:19], v[224:227]
	s_waitcnt lgkmcnt(5)
	v_mfma_f32_16x16x32_f16 v[196:199], v[164:167], v[20:23], v[196:199]
	v_mfma_f32_16x16x32_f16 v[228:231], v[124:127], v[20:23], v[228:231]
	s_waitcnt lgkmcnt(4)
	v_mfma_f32_16x16x32_f16 v[200:203], v[168:171], v[24:27], v[200:203]
	v_mfma_f32_16x16x32_f16 v[232:235], v[128:131], v[24:27], v[232:235]
	s_waitcnt lgkmcnt(3)
	v_mfma_f32_16x16x32_f16 v[204:207], v[172:175], v[28:31], v[204:207]
	v_mfma_f32_16x16x32_f16 v[236:239], v[132:135], v[28:31], v[236:239]
	s_waitcnt lgkmcnt(2)
	v_mfma_f32_16x16x32_f16 v[208:211], v[176:179], v[32:35], v[208:211]
	v_mfma_f32_16x16x32_f16 v[240:243], v[136:139], v[32:35], v[240:243]
	s_waitcnt lgkmcnt(1)
	v_mfma_f32_16x16x32_f16 v[212:215], v[180:183], v[36:39], v[212:215]
	v_mfma_f32_16x16x32_f16 v[244:247], v[140:143], v[36:39], v[244:247]
	s_waitcnt lgkmcnt(0)
	v_mfma_f32_16x16x32_f16 v[216:219], v[184:187], v[40:43], v[216:219]
	v_mfma_f32_16x16x32_f16 v[248:251], v[144:147], v[40:43], v[248:251]
	s_mov_b32 s40, 0x30000
	s_mov_b32 s41, 0x30400
	s_mov_b32 s42, 0x30800
	s_mov_b32 s43, 0x30c00
	buffer_load_dwordx4 v[148:151], v4, s[8:11], s40 offen
	buffer_load_dwordx4 v[152:155], v4, s[8:11], s41 offen
	buffer_load_dwordx4 v[156:159], v4, s[8:11], s42 offen
	buffer_load_dwordx4 v[160:163], v4, s[8:11], s43 offen
	s_mov_b32 s40, 0x31000
	s_mov_b32 s41, 0x31400
	s_mov_b32 s42, 0x31800
	s_mov_b32 s43, 0x31c00
	buffer_load_dwordx4 v[164:167], v4, s[8:11], s40 offen
	buffer_load_dwordx4 v[168:171], v4, s[8:11], s41 offen
	buffer_load_dwordx4 v[172:175], v4, s[8:11], s42 offen
	buffer_load_dwordx4 v[176:179], v4, s[8:11], s43 offen
	s_waitcnt vmcnt(32)
	v_cvt_pkrtz_f16_f32 v12, v44, v46
	v_cvt_pkrtz_f16_f32 v13, v48, v50
	v_cvt_pkrtz_f16_f32 v14, v52, v54
	v_cvt_pkrtz_f16_f32 v15, v56, v58
	v_cvt_pkrtz_f16_f32 v16, v45, v47
	v_cvt_pkrtz_f16_f32 v17, v49, v51
	v_cvt_pkrtz_f16_f32 v18, v53, v55
	v_cvt_pkrtz_f16_f32 v19, v57, v59
	s_mov_b32 s40, 0x1a470
	s_mov_b32 s41, 0x3c100
	s_mov_b32 s42, 0x5dd90
	s_mov_b32 s43, 0x7fa20
	s_mov_b32 s44, 0xa16b0
	s_mov_b32 s45, 0xc3340
	s_mov_b32 s46, 0xe4fd0
	s_mov_b32 s47, 0x106c60
	buffer_load_dwordx2 v[44:45], v3, s[4:7], s40 offen nt
	buffer_load_dwordx2 v[46:47], v3, s[4:7], s41 offen nt
	buffer_load_dwordx2 v[48:49], v3, s[4:7], s42 offen nt
	buffer_load_dwordx2 v[50:51], v3, s[4:7], s43 offen nt
	buffer_load_dwordx2 v[52:53], v3, s[4:7], s44 offen nt
	buffer_load_dwordx2 v[54:55], v3, s[4:7], s45 offen nt
	buffer_load_dwordx2 v[56:57], v3, s[4:7], s46 offen nt
	buffer_load_dwordx2 v[58:59], v3, s[4:7], s47 offen nt
	ds_write_b128 v5, v[12:15] offset:0
	ds_write_b128 v5, v[16:19] offset:2048
	s_waitcnt vmcnt(32)
	v_cvt_pkrtz_f16_f32 v12, v60, v62
	v_cvt_pkrtz_f16_f32 v13, v64, v66
	v_cvt_pkrtz_f16_f32 v14, v68, v70
	v_cvt_pkrtz_f16_f32 v15, v72, v74
	v_cvt_pkrtz_f16_f32 v16, v61, v63
	v_cvt_pkrtz_f16_f32 v17, v65, v67
	v_cvt_pkrtz_f16_f32 v18, v69, v71
	v_cvt_pkrtz_f16_f32 v19, v73, v75
	s_mov_b32 s40, 0x1288f0
	s_mov_b32 s41, 0x14a580
	s_mov_b32 s42, 0x16c210
	s_mov_b32 s43, 0x18dea0
	s_mov_b32 s44, 0x1afb30
	s_mov_b32 s45, 0x1d17c0
	s_mov_b32 s46, 0x1f3450
	s_mov_b32 s47, 0x2150e0
	buffer_load_dwordx2 v[60:61], v3, s[4:7], s40 offen nt
	buffer_load_dwordx2 v[62:63], v3, s[4:7], s41 offen nt
	buffer_load_dwordx2 v[64:65], v3, s[4:7], s42 offen nt
	buffer_load_dwordx2 v[66:67], v3, s[4:7], s43 offen nt
	buffer_load_dwordx2 v[68:69], v3, s[4:7], s44 offen nt
	buffer_load_dwordx2 v[70:71], v3, s[4:7], s45 offen nt
	buffer_load_dwordx2 v[72:73], v3, s[4:7], s46 offen nt
	buffer_load_dwordx2 v[74:75], v3, s[4:7], s47 offen nt
	ds_write_b128 v5, v[12:15] offset:256
	ds_write_b128 v5, v[16:19] offset:2304
	s_waitcnt vmcnt(32)
	v_cvt_pkrtz_f16_f32 v12, v76, v78
	v_cvt_pkrtz_f16_f32 v13, v80, v82
	v_cvt_pkrtz_f16_f32 v14, v84, v86
	v_cvt_pkrtz_f16_f32 v15, v88, v90
	v_cvt_pkrtz_f16_f32 v16, v77, v79
	v_cvt_pkrtz_f16_f32 v17, v81, v83
	v_cvt_pkrtz_f16_f32 v18, v85, v87
	v_cvt_pkrtz_f16_f32 v19, v89, v91
	s_mov_b32 s40, 0x236d70
	s_mov_b32 s41, 0x258a00
	s_mov_b32 s42, 0x27a690
	s_mov_b32 s43, 0x29c320
	s_mov_b32 s44, 0x2bdfb0
	s_mov_b32 s45, 0x2dfc40
	s_mov_b32 s46, 0x3018d0
	s_mov_b32 s47, 0x323560
	buffer_load_dwordx2 v[76:77], v3, s[4:7], s40 offen nt
	buffer_load_dwordx2 v[78:79], v3, s[4:7], s41 offen nt
	buffer_load_dwordx2 v[80:81], v3, s[4:7], s42 offen nt
	buffer_load_dwordx2 v[82:83], v3, s[4:7], s43 offen nt
	buffer_load_dwordx2 v[84:85], v3, s[4:7], s44 offen nt
	buffer_load_dwordx2 v[86:87], v3, s[4:7], s45 offen nt
	buffer_load_dwordx2 v[88:89], v3, s[4:7], s46 offen nt
	buffer_load_dwordx2 v[90:91], v3, s[4:7], s47 offen nt
	ds_write_b128 v5, v[12:15] offset:512
	ds_write_b128 v5, v[16:19] offset:2560
	s_waitcnt vmcnt(32)
	v_cvt_pkrtz_f16_f32 v12, v92, v94
	v_cvt_pkrtz_f16_f32 v13, v96, v98
	v_cvt_pkrtz_f16_f32 v14, v100, v102
	v_cvt_pkrtz_f16_f32 v15, v104, v106
	v_cvt_pkrtz_f16_f32 v16, v93, v95
	v_cvt_pkrtz_f16_f32 v17, v97, v99
	v_cvt_pkrtz_f16_f32 v18, v101, v103
	v_cvt_pkrtz_f16_f32 v19, v105, v107
	s_mov_b32 s40, 0x3451f0
	s_mov_b32 s41, 0x366e80
	s_mov_b32 s42, 0x388b10
	s_mov_b32 s43, 0x3aa7a0
	s_mov_b32 s44, 0x3cc430
	s_mov_b32 s45, 0x3ee0c0
	s_mov_b32 s46, 0x40fd50
	s_mov_b32 s47, 0x4319e0
	buffer_load_dwordx2 v[92:93], v3, s[4:7], s40 offen nt
	buffer_load_dwordx2 v[94:95], v3, s[4:7], s41 offen nt
	buffer_load_dwordx2 v[96:97], v3, s[4:7], s42 offen nt
	buffer_load_dwordx2 v[98:99], v3, s[4:7], s43 offen nt
	buffer_load_dwordx2 v[100:101], v3, s[4:7], s44 offen nt
	buffer_load_dwordx2 v[102:103], v3, s[4:7], s45 offen nt
	buffer_load_dwordx2 v[104:105], v3, s[4:7], s46 offen nt
	buffer_load_dwordx2 v[106:107], v3, s[4:7], s47 offen nt
	ds_write_b128 v5, v[12:15] offset:768
	ds_write_b128 v5, v[16:19] offset:2816
	s_waitcnt lgkmcnt(0)
	s_barrier
	s_waitcnt vmcnt(32)
	ds_write_b128 v254, v[148:151] offset:16384
	ds_write_b128 v254, v[152:155] offset:17408
	s_waitcnt lgkmcnt(0)
	s_barrier
	ds_read_b128 v[180:183], v255 offset:16384
	ds_read_b128 v[184:187], v255 offset:17408
	ds_read_b128 v[12:15], v6 offset:0
	ds_read_b128 v[16:19], v6 offset:2048
	ds_read_b128 v[20:23], v7 offset:0
	ds_read_b128 v[24:27], v7 offset:2048
	ds_read_b128 v[28:31], v8 offset:0
	ds_read_b128 v[32:35], v8 offset:2048
	ds_read_b128 v[36:39], v9 offset:0
	ds_read_b128 v[40:43], v9 offset:2048
	s_waitcnt lgkmcnt(7)
	v_mfma_f32_16x16x32_f16 v[188:191], v[108:111], v[12:15], v[188:191]
	v_mfma_f32_16x16x32_f16 v[220:223], v[148:151], v[12:15], v[220:223]
	s_waitcnt lgkmcnt(6)
	v_mfma_f32_16x16x32_f16 v[192:195], v[112:115], v[16:19], v[192:195]
	v_mfma_f32_16x16x32_f16 v[224:227], v[152:155], v[16:19], v[224:227]
	s_waitcnt lgkmcnt(5)
	v_mfma_f32_16x16x32_f16 v[196:199], v[116:119], v[20:23], v[196:199]
	v_mfma_f32_16x16x32_f16 v[228:231], v[156:159], v[20:23], v[228:231]
	s_waitcnt lgkmcnt(4)
	v_mfma_f32_16x16x32_f16 v[200:203], v[120:123], v[24:27], v[200:203]
	v_mfma_f32_16x16x32_f16 v[232:235], v[160:163], v[24:27], v[232:235]
	s_waitcnt lgkmcnt(3)
	v_mfma_f32_16x16x32_f16 v[204:207], v[124:127], v[28:31], v[204:207]
	v_mfma_f32_16x16x32_f16 v[236:239], v[164:167], v[28:31], v[236:239]
	s_waitcnt lgkmcnt(2)
	v_mfma_f32_16x16x32_f16 v[208:211], v[128:131], v[32:35], v[208:211]
	v_mfma_f32_16x16x32_f16 v[240:243], v[168:171], v[32:35], v[240:243]
	s_waitcnt lgkmcnt(1)
	v_mfma_f32_16x16x32_f16 v[212:215], v[132:135], v[36:39], v[212:215]
	v_mfma_f32_16x16x32_f16 v[244:247], v[172:175], v[36:39], v[244:247]
	s_waitcnt lgkmcnt(0)
	v_mfma_f32_16x16x32_f16 v[216:219], v[136:139], v[40:43], v[216:219]
	v_mfma_f32_16x16x32_f16 v[248:251], v[176:179], v[40:43], v[248:251]
	s_waitcnt vmcnt(24)
	v_cvt_pkrtz_f16_f32 v12, v44, v46
	v_cvt_pkrtz_f16_f32 v13, v48, v50
	v_cvt_pkrtz_f16_f32 v14, v52, v54
	v_cvt_pkrtz_f16_f32 v15, v56, v58
	v_cvt_pkrtz_f16_f32 v16, v45, v47
	v_cvt_pkrtz_f16_f32 v17, v49, v51
	v_cvt_pkrtz_f16_f32 v18, v53, v55
	v_cvt_pkrtz_f16_f32 v19, v57, v59
	s_mov_b32 s40, 0x1e080
	s_mov_b32 s41, 0x3fd10
	s_mov_b32 s42, 0x619a0
	s_mov_b32 s43, 0x83630
	s_mov_b32 s44, 0xa52c0
	s_mov_b32 s45, 0xc6f50
	s_mov_b32 s46, 0xe8be0
	s_mov_b32 s47, 0x10a870
	buffer_load_dwordx2 v[44:45], v3, s[4:7], s40 offen nt
	buffer_load_dwordx2 v[46:47], v3, s[4:7], s41 offen nt
	buffer_load_dwordx2 v[48:49], v3, s[4:7], s42 offen nt
	buffer_load_dwordx2 v[50:51], v3, s[4:7], s43 offen nt
	buffer_load_dwordx2 v[52:53], v3, s[4:7], s44 offen nt
	buffer_load_dwordx2 v[54:55], v3, s[4:7], s45 offen nt
	buffer_load_dwordx2 v[56:57], v3, s[4:7], s46 offen nt
	buffer_load_dwordx2 v[58:59], v3, s[4:7], s47 offen nt
	ds_write_b128 v5, v[12:15] offset:1024
	ds_write_b128 v5, v[16:19] offset:3072
	s_waitcnt vmcnt(24)
	v_cvt_pkrtz_f16_f32 v12, v60, v62
	v_cvt_pkrtz_f16_f32 v13, v64, v66
	v_cvt_pkrtz_f16_f32 v14, v68, v70
	v_cvt_pkrtz_f16_f32 v15, v72, v74
	v_cvt_pkrtz_f16_f32 v16, v61, v63
	v_cvt_pkrtz_f16_f32 v17, v65, v67
	v_cvt_pkrtz_f16_f32 v18, v69, v71
	v_cvt_pkrtz_f16_f32 v19, v73, v75
	s_mov_b32 s40, 0x12c500
	s_mov_b32 s41, 0x14e190
	s_mov_b32 s42, 0x16fe20
	s_mov_b32 s43, 0x191ab0
	s_mov_b32 s44, 0x1b3740
	s_mov_b32 s45, 0x1d53d0
	s_mov_b32 s46, 0x1f7060
	s_mov_b32 s47, 0x218cf0
	buffer_load_dwordx2 v[60:61], v3, s[4:7], s40 offen nt
	buffer_load_dwordx2 v[62:63], v3, s[4:7], s41 offen nt
	buffer_load_dwordx2 v[64:65], v3, s[4:7], s42 offen nt
	buffer_load_dwordx2 v[66:67], v3, s[4:7], s43 offen nt
	buffer_load_dwordx2 v[68:69], v3, s[4:7], s44 offen nt
	buffer_load_dwordx2 v[70:71], v3, s[4:7], s45 offen nt
	buffer_load_dwordx2 v[72:73], v3, s[4:7], s46 offen nt
	buffer_load_dwordx2 v[74:75], v3, s[4:7], s47 offen nt
	ds_write_b128 v5, v[12:15] offset:1280
	ds_write_b128 v5, v[16:19] offset:3328
	s_waitcnt vmcnt(24)
	v_cvt_pkrtz_f16_f32 v12, v76, v78
	v_cvt_pkrtz_f16_f32 v13, v80, v82
	v_cvt_pkrtz_f16_f32 v14, v84, v86
	v_cvt_pkrtz_f16_f32 v15, v88, v90
	v_cvt_pkrtz_f16_f32 v16, v77, v79
	v_cvt_pkrtz_f16_f32 v17, v81, v83
	v_cvt_pkrtz_f16_f32 v18, v85, v87
	v_cvt_pkrtz_f16_f32 v19, v89, v91
	s_mov_b32 s40, 0x23a980
	s_mov_b32 s41, 0x25c610
	s_mov_b32 s42, 0x27e2a0
	s_mov_b32 s43, 0x29ff30
	s_mov_b32 s44, 0x2c1bc0
	s_mov_b32 s45, 0x2e3850
	s_mov_b32 s46, 0x3054e0
	s_mov_b32 s47, 0x327170
	buffer_load_dwordx2 v[76:77], v3, s[4:7], s40 offen nt
	buffer_load_dwordx2 v[78:79], v3, s[4:7], s41 offen nt
	buffer_load_dwordx2 v[80:81], v3, s[4:7], s42 offen nt
	buffer_load_dwordx2 v[82:83], v3, s[4:7], s43 offen nt
	buffer_load_dwordx2 v[84:85], v3, s[4:7], s44 offen nt
	buffer_load_dwordx2 v[86:87], v3, s[4:7], s45 offen nt
	buffer_load_dwordx2 v[88:89], v3, s[4:7], s46 offen nt
	buffer_load_dwordx2 v[90:91], v3, s[4:7], s47 offen nt
	ds_write_b128 v5, v[12:15] offset:1536
	ds_write_b128 v5, v[16:19] offset:3584
	s_waitcnt vmcnt(24)
	v_cvt_pkrtz_f16_f32 v12, v92, v94
	v_cvt_pkrtz_f16_f32 v13, v96, v98
	v_cvt_pkrtz_f16_f32 v14, v100, v102
	v_cvt_pkrtz_f16_f32 v15, v104, v106
	v_cvt_pkrtz_f16_f32 v16, v93, v95
	v_cvt_pkrtz_f16_f32 v17, v97, v99
	v_cvt_pkrtz_f16_f32 v18, v101, v103
	v_cvt_pkrtz_f16_f32 v19, v105, v107
	s_mov_b32 s40, 0x348e00
	s_mov_b32 s41, 0x36aa90
	s_mov_b32 s42, 0x38c720
	s_mov_b32 s43, 0x3ae3b0
	s_mov_b32 s44, 0x3d0040
	s_mov_b32 s45, 0x3f1cd0
	s_mov_b32 s46, 0x413960
	s_mov_b32 s47, 0x4355f0
	buffer_load_dwordx2 v[92:93], v3, s[4:7], s40 offen nt
	buffer_load_dwordx2 v[94:95], v3, s[4:7], s41 offen nt
	buffer_load_dwordx2 v[96:97], v3, s[4:7], s42 offen nt
	buffer_load_dwordx2 v[98:99], v3, s[4:7], s43 offen nt
	buffer_load_dwordx2 v[100:101], v3, s[4:7], s44 offen nt
	buffer_load_dwordx2 v[102:103], v3, s[4:7], s45 offen nt
	buffer_load_dwordx2 v[104:105], v3, s[4:7], s46 offen nt
	buffer_load_dwordx2 v[106:107], v3, s[4:7], s47 offen nt
	ds_write_b128 v5, v[12:15] offset:1792
	ds_write_b128 v5, v[16:19] offset:3840
	s_waitcnt lgkmcnt(0)
	s_barrier
	ds_read_b128 v[12:15], v6 offset:1024
	ds_read_b128 v[16:19], v6 offset:3072
	ds_read_b128 v[20:23], v7 offset:1024
	ds_read_b128 v[24:27], v7 offset:3072
	ds_read_b128 v[28:31], v8 offset:1024
	ds_read_b128 v[32:35], v8 offset:3072
	ds_read_b128 v[36:39], v9 offset:1024
	ds_read_b128 v[40:43], v9 offset:3072
	s_waitcnt lgkmcnt(7)
	v_mfma_f32_16x16x32_f16 v[188:191], v[112:115], v[12:15], v[188:191]
	v_mfma_f32_16x16x32_f16 v[220:223], v[152:155], v[12:15], v[220:223]
	s_waitcnt lgkmcnt(6)
	v_mfma_f32_16x16x32_f16 v[192:195], v[116:119], v[16:19], v[192:195]
	v_mfma_f32_16x16x32_f16 v[224:227], v[156:159], v[16:19], v[224:227]
	s_waitcnt lgkmcnt(5)
	v_mfma_f32_16x16x32_f16 v[196:199], v[120:123], v[20:23], v[196:199]
	v_mfma_f32_16x16x32_f16 v[228:231], v[160:163], v[20:23], v[228:231]
	s_waitcnt lgkmcnt(4)
	v_mfma_f32_16x16x32_f16 v[200:203], v[124:127], v[24:27], v[200:203]
	v_mfma_f32_16x16x32_f16 v[232:235], v[164:167], v[24:27], v[232:235]
	s_waitcnt lgkmcnt(3)
	v_mfma_f32_16x16x32_f16 v[204:207], v[128:131], v[28:31], v[204:207]
	v_mfma_f32_16x16x32_f16 v[236:239], v[168:171], v[28:31], v[236:239]
	s_waitcnt lgkmcnt(2)
	v_mfma_f32_16x16x32_f16 v[208:211], v[132:135], v[32:35], v[208:211]
	v_mfma_f32_16x16x32_f16 v[240:243], v[172:175], v[32:35], v[240:243]
	s_waitcnt lgkmcnt(1)
	v_mfma_f32_16x16x32_f16 v[212:215], v[136:139], v[36:39], v[212:215]
	v_mfma_f32_16x16x32_f16 v[244:247], v[176:179], v[36:39], v[244:247]
	s_waitcnt lgkmcnt(0)
	v_mfma_f32_16x16x32_f16 v[216:219], v[140:143], v[40:43], v[216:219]
	v_mfma_f32_16x16x32_f16 v[248:251], v[180:183], v[40:43], v[248:251]
	s_waitcnt vmcnt(24)
	v_cvt_pkrtz_f16_f32 v12, v44, v46
	v_cvt_pkrtz_f16_f32 v13, v48, v50
	v_cvt_pkrtz_f16_f32 v14, v52, v54
	v_cvt_pkrtz_f16_f32 v15, v56, v58
	v_cvt_pkrtz_f16_f32 v16, v45, v47
	v_cvt_pkrtz_f16_f32 v17, v49, v51
	v_cvt_pkrtz_f16_f32 v18, v53, v55
	v_cvt_pkrtz_f16_f32 v19, v57, v59
	ds_write_b128 v5, v[12:15] offset:0
	ds_write_b128 v5, v[16:19] offset:2048
	s_waitcnt vmcnt(16)
	v_cvt_pkrtz_f16_f32 v12, v60, v62
	v_cvt_pkrtz_f16_f32 v13, v64, v66
	v_cvt_pkrtz_f16_f32 v14, v68, v70
	v_cvt_pkrtz_f16_f32 v15, v72, v74
	v_cvt_pkrtz_f16_f32 v16, v61, v63
	v_cvt_pkrtz_f16_f32 v17, v65, v67
	v_cvt_pkrtz_f16_f32 v18, v69, v71
	v_cvt_pkrtz_f16_f32 v19, v73, v75
	ds_write_b128 v5, v[12:15] offset:256
	ds_write_b128 v5, v[16:19] offset:2304
	s_waitcnt vmcnt(8)
	v_cvt_pkrtz_f16_f32 v12, v76, v78
	v_cvt_pkrtz_f16_f32 v13, v80, v82
	v_cvt_pkrtz_f16_f32 v14, v84, v86
	v_cvt_pkrtz_f16_f32 v15, v88, v90
	v_cvt_pkrtz_f16_f32 v16, v77, v79
	v_cvt_pkrtz_f16_f32 v17, v81, v83
	v_cvt_pkrtz_f16_f32 v18, v85, v87
	v_cvt_pkrtz_f16_f32 v19, v89, v91
	ds_write_b128 v5, v[12:15] offset:512
	ds_write_b128 v5, v[16:19] offset:2560
	s_waitcnt vmcnt(0)
	v_cvt_pkrtz_f16_f32 v12, v92, v94
	v_cvt_pkrtz_f16_f32 v13, v96, v98
	v_cvt_pkrtz_f16_f32 v14, v100, v102
	v_cvt_pkrtz_f16_f32 v15, v104, v106
	v_cvt_pkrtz_f16_f32 v16, v93, v95
	v_cvt_pkrtz_f16_f32 v17, v97, v99
	v_cvt_pkrtz_f16_f32 v18, v101, v103
	v_cvt_pkrtz_f16_f32 v19, v105, v107
	ds_write_b128 v5, v[12:15] offset:768
	ds_write_b128 v5, v[16:19] offset:2816
	s_waitcnt lgkmcnt(0)
	s_barrier
	ds_read_b128 v[12:15], v6 offset:0
	ds_read_b128 v[16:19], v6 offset:2048
	ds_read_b128 v[20:23], v7 offset:0
	ds_read_b128 v[24:27], v7 offset:2048
	ds_read_b128 v[28:31], v8 offset:0
	ds_read_b128 v[32:35], v8 offset:2048
	ds_read_b128 v[36:39], v9 offset:0
	ds_read_b128 v[40:43], v9 offset:2048
	s_waitcnt lgkmcnt(7)
	v_mfma_f32_16x16x32_f16 v[188:191], v[116:119], v[12:15], v[188:191]
	v_mfma_f32_16x16x32_f16 v[220:223], v[156:159], v[12:15], v[220:223]
	s_waitcnt lgkmcnt(6)
	v_mfma_f32_16x16x32_f16 v[192:195], v[120:123], v[16:19], v[192:195]
	v_mfma_f32_16x16x32_f16 v[224:227], v[160:163], v[16:19], v[224:227]
	s_waitcnt lgkmcnt(5)
	v_mfma_f32_16x16x32_f16 v[196:199], v[124:127], v[20:23], v[196:199]
	v_mfma_f32_16x16x32_f16 v[228:231], v[164:167], v[20:23], v[228:231]
	s_waitcnt lgkmcnt(4)
	v_mfma_f32_16x16x32_f16 v[200:203], v[128:131], v[24:27], v[200:203]
	v_mfma_f32_16x16x32_f16 v[232:235], v[168:171], v[24:27], v[232:235]
	s_waitcnt lgkmcnt(3)
	v_mfma_f32_16x16x32_f16 v[204:207], v[132:135], v[28:31], v[204:207]
	v_mfma_f32_16x16x32_f16 v[236:239], v[172:175], v[28:31], v[236:239]
	s_waitcnt lgkmcnt(2)
	v_mfma_f32_16x16x32_f16 v[208:211], v[136:139], v[32:35], v[208:211]
	v_mfma_f32_16x16x32_f16 v[240:243], v[176:179], v[32:35], v[240:243]
	s_waitcnt lgkmcnt(1)
	v_mfma_f32_16x16x32_f16 v[212:215], v[140:143], v[36:39], v[212:215]
	v_mfma_f32_16x16x32_f16 v[244:247], v[180:183], v[36:39], v[244:247]
	s_waitcnt lgkmcnt(0)
	v_mfma_f32_16x16x32_f16 v[216:219], v[144:147], v[40:43], v[216:219]
	v_mfma_f32_16x16x32_f16 v[248:251], v[184:187], v[40:43], v[248:251]
	s_nop 7
	s_nop 3
	v_and_b32_e32 v10, 1, v0
	v_cmp_eq_u32_e32 vcc, 1, v10
	s_nop 1
	v_cndmask_b32_e32 v188, v188, v220, vcc
	v_cndmask_b32_e32 v189, v189, v221, vcc
	v_cndmask_b32_e32 v190, v190, v222, vcc
	v_cndmask_b32_e32 v191, v191, v223, vcc
	v_cndmask_b32_e32 v192, v192, v224, vcc
	v_cndmask_b32_e32 v193, v193, v225, vcc
	v_cndmask_b32_e32 v194, v194, v226, vcc
	v_cndmask_b32_e32 v195, v195, v227, vcc
	v_cndmask_b32_e32 v196, v196, v228, vcc
	v_cndmask_b32_e32 v197, v197, v229, vcc
	v_cndmask_b32_e32 v198, v198, v230, vcc
	v_cndmask_b32_e32 v199, v199, v231, vcc
	v_cndmask_b32_e32 v200, v200, v232, vcc
	v_cndmask_b32_e32 v201, v201, v233, vcc
	v_cndmask_b32_e32 v202, v202, v234, vcc
	v_cndmask_b32_e32 v203, v203, v235, vcc
	v_cndmask_b32_e32 v204, v204, v236, vcc
	v_cndmask_b32_e32 v205, v205, v237, vcc
	v_cndmask_b32_e32 v206, v206, v238, vcc
	v_cndmask_b32_e32 v207, v207, v239, vcc
	v_cndmask_b32_e32 v208, v208, v240, vcc
	v_cndmask_b32_e32 v209, v209, v241, vcc
	v_cndmask_b32_e32 v210, v210, v242, vcc
	v_cndmask_b32_e32 v211, v211, v243, vcc
	v_cndmask_b32_e32 v212, v212, v244, vcc
	v_cndmask_b32_e32 v213, v213, v245, vcc
	v_cndmask_b32_e32 v214, v214, v246, vcc
	v_cndmask_b32_e32 v215, v215, v247, vcc
	v_cndmask_b32_e32 v216, v216, v248, vcc
	v_cndmask_b32_e32 v217, v217, v249, vcc
	v_cndmask_b32_e32 v218, v218, v250, vcc
	v_cndmask_b32_e32 v219, v219, v251, vcc
	s_barrier
	v_lshrrev_b32_e32 v10, 4, v2
	v_lshlrev_b32_e32 v10, 6, v10
	v_and_b32_e32 v12, 15, v2
	v_add_u32_e32 v10, v10, v12
	v_mul_u32_u24_e32 v10, 0x108, v10
	v_lshl_add_u32 v10, v1, 5, v10
	ds_write_b32 v10, v188 offset:0
	ds_write_b32 v10, v189 offset:4224
	ds_write_b32 v10, v190 offset:8448
	ds_write_b32 v10, v191 offset:12672
	ds_write_b32 v10, v192 offset:4
	ds_write_b32 v10, v193 offset:4228
	ds_write_b32 v10, v194 offset:8452
	ds_write_b32 v10, v195 offset:12676
	s_waitcnt lgkmcnt(4)
	ds_write_b32 v10, v196 offset:8
	ds_write_b32 v10, v197 offset:4232
	ds_write_b32 v10, v198 offset:8456
	ds_write_b32 v10, v199 offset:12680
	ds_write_b32 v10, v200 offset:12
	ds_write_b32 v10, v201 offset:4236
	ds_write_b32 v10, v202 offset:8460
	ds_write_b32 v10, v203 offset:12684
	s_waitcnt lgkmcnt(4)
	ds_write_b32 v10, v204 offset:16
	ds_write_b32 v10, v205 offset:4240
	ds_write_b32 v10, v206 offset:8464
	ds_write_b32 v10, v207 offset:12688
	ds_write_b32 v10, v208 offset:20
	ds_write_b32 v10, v209 offset:4244
	ds_write_b32 v10, v210 offset:8468
	ds_write_b32 v10, v211 offset:12692
	s_waitcnt lgkmcnt(4)
	ds_write_b32 v10, v212 offset:24
	ds_write_b32 v10, v213 offset:4248
	ds_write_b32 v10, v214 offset:8472
	ds_write_b32 v10, v215 offset:12696
	ds_write_b32 v10, v216 offset:28
	ds_write_b32 v10, v217 offset:4252
	ds_write_b32 v10, v218 offset:8476
	ds_write_b32 v10, v219 offset:12700
	s_waitcnt lgkmcnt(0)
	s_barrier
	v_lshrrev_b32_e32 v12, 5, v0
	v_mul_u32_u24_e32 v12, 0x108, v12
	v_and_b32_e32 v13, 31, v0
	v_lshl_add_u32 v12, v13, 3, v12
	ds_read_b64 v[44:45], v12 offset:0
	ds_read_b64 v[46:47], v12 offset:4224
	ds_read_b64 v[48:49], v12 offset:8448
	ds_read_b64 v[50:51], v12 offset:12672
	ds_read_b64 v[52:53], v12 offset:16896
	ds_read_b64 v[54:55], v12 offset:21120
	ds_read_b64 v[56:57], v12 offset:25344
	ds_read_b64 v[58:59], v12 offset:29568
	s_waitcnt lgkmcnt(7)
	v_add_f32_e32 v44, v252, v44
	v_add_f32_e32 v45, v253, v45
	s_mov_b32 s40, 0x0
	buffer_store_dwordx2 v[44:45], v11, s[32:35], s40 offen nt
	s_waitcnt lgkmcnt(6)
	v_add_f32_e32 v46, v252, v46
	v_add_f32_e32 v47, v253, v47
	s_mov_b32 s41, 0xf0400
	buffer_store_dwordx2 v[46:47], v11, s[32:35], s41 offen nt
	s_waitcnt lgkmcnt(5)
	v_add_f32_e32 v48, v252, v48
	v_add_f32_e32 v49, v253, v49
	s_mov_b32 s42, 0x1e0800
	buffer_store_dwordx2 v[48:49], v11, s[32:35], s42 offen nt
	s_waitcnt lgkmcnt(4)
	v_add_f32_e32 v50, v252, v50
	v_add_f32_e32 v51, v253, v51
	s_mov_b32 s43, 0x2d0c00
	buffer_store_dwordx2 v[50:51], v11, s[32:35], s43 offen nt
	s_waitcnt lgkmcnt(3)
	v_add_f32_e32 v52, v252, v52
	v_add_f32_e32 v53, v253, v53
	s_mov_b32 s44, 0x3c1000
	buffer_store_dwordx2 v[52:53], v11, s[32:35], s44 offen nt
	s_waitcnt lgkmcnt(2)
	v_add_f32_e32 v54, v252, v54
	v_add_f32_e32 v55, v253, v55
	s_mov_b32 s45, 0x4b1400
	buffer_store_dwordx2 v[54:55], v11, s[32:35], s45 offen nt
	s_waitcnt lgkmcnt(1)
	v_add_f32_e32 v56, v252, v56
	v_add_f32_e32 v57, v253, v57
	s_mov_b32 s46, 0x5a1800
	buffer_store_dwordx2 v[56:57], v11, s[32:35], s46 offen nt
	s_waitcnt lgkmcnt(0)
	v_add_f32_e32 v58, v252, v58
	v_add_f32_e32 v59, v253, v59
	s_mov_b32 s47, 0x691c00
	buffer_store_dwordx2 v[58:59], v11, s[32:35], s47 offen nt
	ds_read_b64 v[60:61], v12 offset:33792
	ds_read_b64 v[62:63], v12 offset:38016
	ds_read_b64 v[64:65], v12 offset:42240
	ds_read_b64 v[66:67], v12 offset:46464
	ds_read_b64 v[68:69], v12 offset:50688
	ds_read_b64 v[70:71], v12 offset:54912
	ds_read_b64 v[72:73], v12 offset:59136
	ds_read_b64 v[74:75], v12 offset:63360
	s_waitcnt lgkmcnt(7)
	v_add_f32_e32 v60, v252, v60
	v_add_f32_e32 v61, v253, v61
	s_mov_b32 s40, 0x782000
	buffer_store_dwordx2 v[60:61], v11, s[32:35], s40 offen nt
	s_waitcnt lgkmcnt(6)
	v_add_f32_e32 v62, v252, v62
	v_add_f32_e32 v63, v253, v63
	s_mov_b32 s41, 0x872400
	buffer_store_dwordx2 v[62:63], v11, s[32:35], s41 offen nt
	s_waitcnt lgkmcnt(5)
	v_add_f32_e32 v64, v252, v64
	v_add_f32_e32 v65, v253, v65
	s_mov_b32 s42, 0x962800
	buffer_store_dwordx2 v[64:65], v11, s[32:35], s42 offen nt
	s_waitcnt lgkmcnt(4)
	v_add_f32_e32 v66, v252, v66
	v_add_f32_e32 v67, v253, v67
	s_mov_b32 s43, 0xa52c00
	buffer_store_dwordx2 v[66:67], v11, s[32:35], s43 offen nt
	s_waitcnt lgkmcnt(3)
	v_add_f32_e32 v68, v252, v68
	v_add_f32_e32 v69, v253, v69
	s_mov_b32 s44, 0xb43000
	buffer_store_dwordx2 v[68:69], v11, s[32:35], s44 offen nt
	s_waitcnt lgkmcnt(2)
	v_add_f32_e32 v70, v252, v70
	v_add_f32_e32 v71, v253, v71
	s_mov_b32 s45, 0xc33400
	buffer_store_dwordx2 v[70:71], v11, s[32:35], s45 offen nt
	s_waitcnt lgkmcnt(1)
	v_add_f32_e32 v72, v252, v72
	v_add_f32_e32 v73, v253, v73
	s_mov_b32 s46, 0xd23800
	buffer_store_dwordx2 v[72:73], v11, s[32:35], s46 offen nt
	s_waitcnt lgkmcnt(0)
	v_add_f32_e32 v74, v252, v74
	v_add_f32_e32 v75, v253, v75
	s_mov_b32 s47, 0xe13c00
	buffer_store_dwordx2 v[74:75], v11, s[32:35], s47 offen nt
	s_endpgm

	.amdhsa_kernel _Z11pwconv_mfmaPKfPK15HIP_vector_typeIjLj4EES0_Pf
		.amdhsa_group_segment_fixed_size 163840
		.amdhsa_private_segment_fixed_size 0
		.amdhsa_kernarg_size 32
		.amdhsa_user_sgpr_count 2
		.amdhsa_user_sgpr_dispatch_ptr 0
		.amdhsa_user_sgpr_queue_ptr 0
		.amdhsa_user_sgpr_kernarg_segment_ptr 1
		.amdhsa_user_sgpr_dispatch_id 0
		.amdhsa_user_sgpr_kernarg_preload_length 0
		.amdhsa_user_sgpr_kernarg_preload_offset 0
		.amdhsa_user_sgpr_private_segment_size 0
		.amdhsa_uses_dynamic_stack 0
		.amdhsa_enable_private_segment 0
		.amdhsa_system_sgpr_workgroup_id_x 1
		.amdhsa_system_sgpr_workgroup_id_y 0
		.amdhsa_system_sgpr_workgroup_id_z 0
		.amdhsa_system_sgpr_workgroup_info 0
		.amdhsa_system_vgpr_workitem_id 0
		.amdhsa_next_free_vgpr 256
		.amdhsa_next_free_sgpr 96
		.amdhsa_accum_offset 256
		.amdhsa_reserve_vcc 1
		.amdhsa_float_round_mode_32 0
		.amdhsa_float_round_mode_16_64 0
		.amdhsa_float_denorm_mode_32 3
		.amdhsa_float_denorm_mode_16_64 3
		.amdhsa_dx10_clamp 1
		.amdhsa_ieee_mode 1
		.amdhsa_fp16_overflow 0
		.amdhsa_tg_split 0
		.amdhsa_exception_fp_ieee_invalid_op 0
		.amdhsa_exception_fp_denorm_src 0
		.amdhsa_exception_fp_ieee_div_zero 0
		.amdhsa_exception_fp_ieee_overflow 0
		.amdhsa_exception_fp_ieee_underflow 0
		.amdhsa_exception_fp_ieee_inexact 0
		.amdhsa_exception_int_div_zero 0
	.end_amdhsa_kernel

.Lfunc_end1:
	.size	_Z11pwconv_mfmaPKfPK15HIP_vector_typeIjLj4EES0_Pf, .Lfunc_end1-_Z11pwconv_mfmaPKfPK15HIP_vector_typeIjLj4EES0_Pf
	.set _Z11pwconv_mfmaPKfPK15HIP_vector_typeIjLj4EES0_Pf.num_vgpr, 256
	.set _Z11pwconv_mfmaPKfPK15HIP_vector_typeIjLj4EES0_Pf.num_agpr, 0
	.set _Z11pwconv_mfmaPKfPK15HIP_vector_typeIjLj4EES0_Pf.numbered_sgpr, 48
	.set _Z11pwconv_mfmaPKfPK15HIP_vector_typeIjLj4EES0_Pf.num_named_barrier, 0
	.set _Z11pwconv_mfmaPKfPK15HIP_vector_typeIjLj4EES0_Pf.private_seg_size, 0
	.set _Z11pwconv_mfmaPKfPK15HIP_vector_typeIjLj4EES0_Pf.uses_vcc, 1
	.set _Z11pwconv_mfmaPKfPK15HIP_vector_typeIjLj4EES0_Pf.uses_flat_scratch, 0
	.set _Z11pwconv_mfmaPKfPK15HIP_vector_typeIjLj4EES0_Pf.has_dyn_sized_stack, 0
	.set _Z11pwconv_mfmaPKfPK15HIP_vector_typeIjLj4EES0_Pf.has_recursion, 0
	.set _Z11pwconv_mfmaPKfPK15HIP_vector_typeIjLj4EES0_Pf.has_indirect_call, 0

amdhsa.kernels:
  - .agpr_count:     0
    .args:
      - .actual_access:  read_only
        .address_space:  global
        .offset:         0
        .size:           8
        .value_kind:     global_buffer
      - .actual_access:  write_only
        .address_space:  global
        .offset:         8
        .size:           8
        .value_kind:     global_buffer
    .group_segment_fixed_size: 34816
    .kernarg_segment_align: 8
    .kernarg_segment_size: 16
    .language:       OpenCL C
    .language_version:
      - 2
      - 0
    .max_flat_workgroup_size: 256
    .name:           _Z7xform_xPKfP15HIP_vector_typeIjLj4EE
    .private_segment_fixed_size: 0
    .sgpr_count:     14
    .sgpr_spill_count: 0
    .symbol:         _Z7xform_xPKfP15HIP_vector_typeIjLj4EE.kd
    .uniform_work_group_size: 1
    .uses_dynamic_stack: false
    .vgpr_count:     42
    .vgpr_spill_count: 0
    .wavefront_size: 64
  - .agpr_count:     0
    .args:
      - .actual_access:  read_only
        .address_space:  global
        .offset:         0
        .size:           8
        .value_kind:     global_buffer
      - .actual_access:  read_only
        .address_space:  global
        .offset:         8
        .size:           8
        .value_kind:     global_buffer
      - .actual_access:  read_only
        .address_space:  global
        .offset:         16
        .size:           8
        .value_kind:     global_buffer
      - .actual_access:  write_only
        .address_space:  global
        .offset:         24
        .size:           8
        .value_kind:     global_buffer
    .group_segment_fixed_size: 163840
    .kernarg_segment_align: 8
    .kernarg_segment_size: 32
    .language:       OpenCL C
    .language_version:
      - 2
      - 0
    .max_flat_workgroup_size: 512
    .name:           _Z11pwconv_mfmaPKfPK15HIP_vector_typeIjLj4EES0_Pf
    .private_segment_fixed_size: 0
    .sgpr_count:     54
    .sgpr_spill_count: 0
    .symbol:         _Z11pwconv_mfmaPKfPK15HIP_vector_typeIjLj4EES0_Pf.kd
    .uniform_work_group_size: 1
    .uses_dynamic_stack: false
    .vgpr_count:     256
    .vgpr_spill_count: 0
    .wavefront_size: 64
